# speedup vs baseline: 1.0239x; 1.0067x over previous
.LBB7_3:
	s_ashr_i32 s44, s23, 31
	s_xor_b32 s44, s44, s25
	s_abs_i32 s45, s23
	s_mul_hi_u32 s48, s45, s26
	s_mul_i32 s49, s48, s24
	s_sub_i32 s45, s45, s49
	s_add_i32 s49, s48, 1
	s_sub_i32 s46, s45, s24
	s_cmp_ge_u32 s45, s24
	s_cselect_b32 s48, s49, s48
	s_cselect_b32 s45, s46, s45
	s_add_i32 s49, s48, 1
	s_cmp_ge_u32 s45, s24
	s_cselect_b32 s45, s49, s48
	s_xor_b32 s45, s45, s44
	s_sub_i32 s44, s45, s44
	s_mul_i32 s45, s44, s21
	s_sub_i32 s47, s23, s45
	s_lshl_b32 s48, s47, 7
	s_lshl_b32 s46, s44, 7
	s_ashr_i32 s49, s48, 31
	v_or_b32_e32 v152, s46, v1
	v_lshl_add_u64 v[154:155], s[48:49], 1, v[70:71]
	v_mad_i64_i32 v[156:157], s[50:51], v152, s29, v[154:155]
	v_lshl_add_u64 v[158:159], s[48:49], 2, v[68:69]
	v_or_b32_e32 v153, 32, v152
	global_load_dwordx4 v[160:163], v[156:157], off
	v_mad_i64_i32 v[184:185], s[50:51], v153, s29, v[154:155]
	v_or_b32_e32 v153, 64, v152
	global_load_dwordx4 v[176:179], v[158:159], off
	global_load_dwordx4 v[180:183], v[158:159], off offset:16
	v_mad_i64_i32 v[186:187], s[50:51], v153, s29, v[154:155]
	v_or_b32_e32 v153, 0x60, v152
	global_load_dwordx4 v[164:167], v[184:185], off
	v_mad_i64_i32 v[188:189], s[50:51], v153, s29, v[154:155]
	global_load_dwordx4 v[168:171], v[186:187], off
	s_nop 0
	global_load_dwordx4 v[172:175], v[188:189], off
	v_add_u32_e32 v67, v80, v77
	s_waitcnt vmcnt(14)
	s_barrier
	s_waitcnt lgkmcnt(0)
	ds_read_b128 v[2:5], v67 offset:16384
	v_add_u32_e32 v109, v79, v77
	ds_read_b128 v[6:9], v109
	ds_read_b128 v[10:13], v109 offset:4096
	ds_read_b128 v[14:17], v67 offset:20480
	v_add_u32_e32 v126, v80, v76
	ds_read_b128 v[34:37], v126 offset:16384
	v_add_u32_e32 v127, v79, v76
	s_waitcnt lgkmcnt(3)
	v_mfma_f32_32x32x16_f16 v[50:65], v[2:5], v[6:9], 0
	ds_read_b128 v[110:113], v127
	ds_read_b128 v[114:117], v127 offset:4096
	ds_read_b128 v[118:121], v126 offset:20480
	v_readfirstlane_b32 s2, v0
	s_lshl_b32 s19, s27, 15
	s_lshl_b32 s2, s2, 4
	s_add_i32 s1, s19, 0
	s_and_b32 s31, s2, 0xfffffc00
	s_add_i32 s1, s1, s31
	s_waitcnt lgkmcnt(5)
	v_mfma_f32_32x32x16_f16 v[18:33], v[2:5], v[10:13], 0
	s_mov_b32 m0, s1
	s_add_i32 s2, s1, 0x2000
	buffer_load_dwordx4 v72, s[4:7], s0 offen lds
	s_mov_b32 m0, s2
	s_add_i32 s3, s1, 0x4000
	buffer_load_dwordx4 v74, s[4:7], s0 offen lds
	s_mov_b32 s14, s10
	s_waitcnt lgkmcnt(2)
	v_mfma_f32_32x32x16_f16 v[50:65], v[34:37], v[110:113], v[50:65]
	s_mov_b32 s15, s11
	s_mov_b32 m0, s3
	s_add_i32 s18, s1, 0x6000
	buffer_load_dwordx4 v73, s[12:15], s0 offen lds
	s_mov_b32 m0, s18
	s_add_i32 s33, s19, 0x8000
	buffer_load_dwordx4 v75, s[12:15], s0 offen lds
	s_waitcnt lgkmcnt(1)
	v_mfma_f32_32x32x16_f16 v[18:33], v[34:37], v[114:117], v[18:33]
	s_waitcnt vmcnt(14)
	s_barrier
	s_and_b32 s33, s33, 0x18000
	s_add_i32 s33, s33, 0
	s_add_i32 s33, s33, s31
	s_add_i32 s34, s0, 0x80
	s_mov_b32 m0, s33
	v_mfma_f32_32x32x16_f16 v[34:49], v[14:17], v[6:9], 0
	v_add_u32_e32 v128, v81, v77
	v_add_u32_e32 v129, v82, v77
	v_add_u32_e32 v130, v81, v76
	v_add_u32_e32 v131, v82, v76
	s_xor_b32 s19, s19, 0x10000
	v_add_u32_e32 v134, v83, v77
	v_add_u32_e32 v138, v84, v77
	v_mfma_f32_32x32x16_f16 v[2:17], v[14:17], v[10:13], 0
	v_add_u32_e32 v142, v83, v76
	v_add_u32_e32 v146, v84, v76
	s_waitcnt lgkmcnt(0)
	v_mfma_f32_32x32x16_f16 v[34:49], v[118:121], v[110:113], v[34:49]
	v_mfma_f32_32x32x16_f16 v[2:17], v[118:121], v[114:117], v[2:17]
	ds_read_b128 v[110:113], v67 offset:49152
	ds_read_b128 v[114:117], v109 offset:32768
	ds_read_b128 v[118:121], v109 offset:36864
	ds_read_b128 v[122:125], v67 offset:53248
	s_waitcnt lgkmcnt(2)
	v_mfma_f32_32x32x16_f16 v[50:65], v[110:113], v[114:117], v[50:65]
	s_waitcnt lgkmcnt(1)
	v_mfma_f32_32x32x16_f16 v[18:33], v[110:113], v[118:121], v[18:33]
	s_waitcnt lgkmcnt(0)
	v_mfma_f32_32x32x16_f16 v[34:49], v[122:125], v[114:117], v[34:49]
	v_mfma_f32_32x32x16_f16 v[2:17], v[122:125], v[118:121], v[2:17]
	ds_read_b128 v[110:113], v126 offset:49152
	ds_read_b128 v[114:117], v127 offset:32768
	ds_read_b128 v[118:121], v127 offset:36864
	ds_read_b128 v[122:125], v126 offset:53248
	buffer_load_dwordx4 v72, s[4:7], s34 offen lds
	s_add_i32 m0, s33, 0x2000
	s_nop 0
	buffer_load_dwordx4 v74, s[4:7], s34 offen lds
	s_add_i32 m0, s33, 0x4000
	s_nop 0
	buffer_load_dwordx4 v73, s[12:15], s34 offen lds
	s_add_i32 m0, s33, 0x6000
	s_waitcnt lgkmcnt(2)
	v_mfma_f32_32x32x16_f16 v[50:65], v[110:113], v[114:117], v[50:65]
	buffer_load_dwordx4 v75, s[12:15], s34 offen lds
	s_waitcnt vmcnt(14)
	s_barrier
	s_add_i32 s33, s19, 0
	s_add_i32 s33, s33, s31
	s_add_i32 s34, s0, 0x100
	s_mov_b32 m0, s33
	s_waitcnt lgkmcnt(1)
	v_mfma_f32_32x32x16_f16 v[18:33], v[110:113], v[118:121], v[18:33]
	ds_read_b128 v[110:113], v96
	s_add_i32 s19, s19, 0x8000
	s_and_b32 s19, s19, 0x18000
	s_add_i32 s19, s19, 0
	s_add_i32 s19, s19, s31
	s_add_i32 s31, s0, 0x180
	s_waitcnt lgkmcnt(1)
	v_mfma_f32_32x32x16_f16 v[34:49], v[122:125], v[114:117], v[34:49]
	v_mfma_f32_32x32x16_f16 v[2:17], v[122:125], v[118:121], v[2:17]
	ds_read_b128 v[114:117], v128
	ds_read_b128 v[118:121], v128 offset:4096
	ds_read_b128 v[122:125], v129 offset:4096
	s_waitcnt lgkmcnt(2)
	v_mfma_f32_32x32x16_f16 v[50:65], v[110:113], v[114:117], v[50:65]
	s_waitcnt lgkmcnt(1)
	v_mfma_f32_32x32x16_f16 v[18:33], v[110:113], v[118:121], v[18:33]
	ds_read_b128 v[110:113], v97
	s_waitcnt lgkmcnt(1)
	v_mfma_f32_32x32x16_f16 v[34:49], v[122:125], v[114:117], v[34:49]
	v_mfma_f32_32x32x16_f16 v[2:17], v[122:125], v[118:121], v[2:17]
	ds_read_b128 v[114:117], v130
	ds_read_b128 v[118:121], v130 offset:4096
	ds_read_b128 v[122:125], v131 offset:4096
	buffer_load_dwordx4 v72, s[4:7], s34 offen lds
	s_add_i32 m0, s33, 0x2000
	s_nop 0
	buffer_load_dwordx4 v74, s[4:7], s34 offen lds
	s_add_i32 m0, s33, 0x4000
	s_waitcnt lgkmcnt(2)
	v_mfma_f32_32x32x16_f16 v[50:65], v[110:113], v[114:117], v[50:65]
	buffer_load_dwordx4 v73, s[12:15], s34 offen lds
	s_add_i32 m0, s33, 0x6000
	s_nop 0
	buffer_load_dwordx4 v75, s[12:15], s34 offen lds
	s_waitcnt vmcnt(8)
	s_barrier
	s_mov_b32 m0, s19
	s_waitcnt lgkmcnt(1)
	v_mfma_f32_32x32x16_f16 v[18:33], v[110:113], v[118:121], v[18:33]
	ds_read_b128 v[110:113], v98
	s_waitcnt lgkmcnt(1)
	v_mfma_f32_32x32x16_f16 v[34:49], v[122:125], v[114:117], v[34:49]
	v_mfma_f32_32x32x16_f16 v[2:17], v[122:125], v[118:121], v[2:17]
	ds_read_b128 v[114:117], v134
	ds_read_b128 v[118:121], v134 offset:4096
	ds_read_b128 v[122:125], v138 offset:4096
	s_waitcnt lgkmcnt(2)
	v_mfma_f32_32x32x16_f16 v[50:65], v[110:113], v[114:117], v[50:65]
	s_waitcnt lgkmcnt(1)
	v_mfma_f32_32x32x16_f16 v[18:33], v[110:113], v[118:121], v[18:33]
	ds_read_b128 v[110:113], v99
	s_waitcnt lgkmcnt(1)
	v_mfma_f32_32x32x16_f16 v[34:49], v[122:125], v[114:117], v[34:49]
	v_mfma_f32_32x32x16_f16 v[2:17], v[122:125], v[118:121], v[2:17]
	ds_read_b128 v[114:117], v142
	ds_read_b128 v[118:121], v142 offset:4096
	ds_read_b128 v[122:125], v146 offset:4096
	buffer_load_dwordx4 v72, s[4:7], s31 offen lds
	s_add_i32 m0, s19, 0x2000
	s_nop 0
	buffer_load_dwordx4 v74, s[4:7], s31 offen lds
	s_add_i32 m0, s19, 0x4000
	s_waitcnt lgkmcnt(2)
	v_mfma_f32_32x32x16_f16 v[50:65], v[110:113], v[114:117], v[50:65]
	buffer_load_dwordx4 v73, s[12:15], s31 offen lds
	s_add_i32 m0, s19, 0x6000
	s_nop 0
	buffer_load_dwordx4 v75, s[12:15], s31 offen lds
	s_waitcnt vmcnt(8)
	s_barrier
	s_add_i32 s31, s0, 0x200
	s_waitcnt lgkmcnt(1)
	v_mfma_f32_32x32x16_f16 v[18:33], v[110:113], v[118:121], v[18:33]
	s_mov_b32 m0, s1
	s_abs_i32 s1, s23
	s_ashr_i32 s0, s23, 31
	s_xor_b32 s0, s0, s25
	s_waitcnt lgkmcnt(0)
	v_mfma_f32_32x32x16_f16 v[2:17], v[122:125], v[118:121], v[2:17]
	v_mfma_f32_32x32x16_f16 v[34:49], v[122:125], v[114:117], v[34:49]
	ds_read_b128 v[110:113], v67 offset:16384
	ds_read_b128 v[114:117], v109
	ds_read_b128 v[118:121], v109 offset:4096
	ds_read_b128 v[122:125], v67 offset:20480
	s_waitcnt lgkmcnt(2)
	v_mfma_f32_32x32x16_f16 v[50:65], v[110:113], v[114:117], v[50:65]
	s_waitcnt lgkmcnt(1)
	v_mfma_f32_32x32x16_f16 v[18:33], v[110:113], v[118:121], v[18:33]
	s_waitcnt lgkmcnt(0)
	v_mfma_f32_32x32x16_f16 v[2:17], v[122:125], v[118:121], v[2:17]
	v_mfma_f32_32x32x16_f16 v[34:49], v[122:125], v[114:117], v[34:49]
	ds_read_b128 v[110:113], v126 offset:16384
	ds_read_b128 v[114:117], v127
	ds_read_b128 v[118:121], v127 offset:4096
	ds_read_b128 v[122:125], v126 offset:20480
	buffer_load_dwordx4 v72, s[4:7], s31 offen lds
	s_mov_b32 m0, s2
	s_mul_hi_u32 s2, s1, s26
	buffer_load_dwordx4 v74, s[4:7], s31 offen lds
	s_mov_b32 m0, s3
	s_mul_i32 s3, s2, s24
	s_waitcnt lgkmcnt(2)
	v_mfma_f32_32x32x16_f16 v[50:65], v[110:113], v[114:117], v[50:65]
	buffer_load_dwordx4 v73, s[12:15], s31 offen lds
	s_mov_b32 m0, s18
	s_sub_i32 s1, s1, s3
	buffer_load_dwordx4 v75, s[12:15], s31 offen lds
	s_waitcnt vmcnt(8)
	s_barrier
	s_add_i32 s3, s2, 1
	s_waitcnt lgkmcnt(1)
	v_mfma_f32_32x32x16_f16 v[18:33], v[110:113], v[118:121], v[18:33]
	s_sub_i32 s14, s1, s24
	s_cmp_ge_u32 s1, s24
	s_cselect_b32 s2, s3, s2
	s_cselect_b32 s1, s14, s1
	s_add_i32 s3, s2, 1
	s_cmp_ge_u32 s1, s24
	s_cselect_b32 s1, s3, s2
	s_waitcnt lgkmcnt(0)
	v_mfma_f32_32x32x16_f16 v[2:17], v[122:125], v[118:121], v[2:17]
	s_xor_b32 s1, s1, s0
	s_sub_i32 s0, s1, s0
	s_mul_i32 s1, s0, s21
	s_sub_i32 s15, s23, s1
	s_lshl_b32 s2, s15, 7
	s_lshl_b32 s14, s0, 7
	s_ashr_i32 s3, s2, 31
	v_mfma_f32_32x32x16_f16 v[34:49], v[122:125], v[114:117], v[34:49]
	ds_read_b128 v[110:113], v67 offset:49152
	ds_read_b128 v[114:117], v109 offset:32768
	ds_read_b128 v[118:121], v109 offset:36864
	ds_read_b128 v[122:125], v67 offset:53248
	s_waitcnt lgkmcnt(2)
	v_mfma_f32_32x32x16_f16 v[50:65], v[110:113], v[114:117], v[50:65]
	s_waitcnt lgkmcnt(1)
	v_mfma_f32_32x32x16_f16 v[18:33], v[110:113], v[118:121], v[18:33]
	s_waitcnt lgkmcnt(0)
	v_mfma_f32_32x32x16_f16 v[2:17], v[122:125], v[118:121], v[2:17]
	v_mfma_f32_32x32x16_f16 v[34:49], v[122:125], v[114:117], v[34:49]
	ds_read_b128 v[110:113], v126 offset:49152
	ds_read_b128 v[114:117], v127 offset:32768
	ds_read_b128 v[118:121], v127 offset:36864
	ds_read_b128 v[122:125], v126 offset:53248
	s_waitcnt vmcnt(4)
	s_barrier
	s_waitcnt lgkmcnt(2)
	v_mfma_f32_32x32x16_f16 v[50:65], v[110:113], v[114:117], v[50:65]
	s_waitcnt lgkmcnt(1)
	v_mfma_f32_32x32x16_f16 v[18:33], v[110:113], v[118:121], v[18:33]
	s_waitcnt lgkmcnt(0)
	v_mfma_f32_32x32x16_f16 v[2:17], v[122:125], v[118:121], v[2:17]
	v_mfma_f32_32x32x16_f16 v[34:49], v[122:125], v[114:117], v[34:49]
	ds_read_b128 v[110:113], v96
	ds_read_b128 v[114:117], v128
	ds_read_b128 v[118:121], v128 offset:4096
	ds_read_b128 v[122:125], v129 offset:4096
	s_waitcnt lgkmcnt(2)
	v_mfma_f32_32x32x16_f16 v[50:65], v[110:113], v[114:117], v[50:65]
	s_waitcnt lgkmcnt(1)
	v_mfma_f32_32x32x16_f16 v[18:33], v[110:113], v[118:121], v[18:33]
	s_waitcnt lgkmcnt(0)
	v_mfma_f32_32x32x16_f16 v[2:17], v[122:125], v[118:121], v[2:17]
	v_mfma_f32_32x32x16_f16 v[34:49], v[122:125], v[114:117], v[34:49]
	ds_read_b128 v[110:113], v97
	ds_read_b128 v[114:117], v130
	ds_read_b128 v[126:129], v130 offset:4096
	ds_read_b128 v[130:133], v131 offset:4096
	s_waitcnt vmcnt(0)
	s_barrier
	s_waitcnt lgkmcnt(2)
	v_mfma_f32_32x32x16_f16 v[50:65], v[110:113], v[114:117], v[50:65]
	s_waitcnt lgkmcnt(1)
	v_mfma_f32_32x32x16_f16 v[18:33], v[110:113], v[126:129], v[18:33]
	s_waitcnt lgkmcnt(0)
	v_mfma_f32_32x32x16_f16 v[2:17], v[130:133], v[126:129], v[2:17]
	v_mfma_f32_32x32x16_f16 v[34:49], v[130:133], v[114:117], v[34:49]
	ds_read_b128 v[110:113], v98
	ds_read_b128 v[114:117], v134
	ds_read_b128 v[134:137], v134 offset:4096
	ds_read_b128 v[138:141], v138 offset:4096
	s_waitcnt lgkmcnt(2)
	v_mfma_f32_32x32x16_f16 v[50:65], v[110:113], v[114:117], v[50:65]
	s_waitcnt lgkmcnt(1)
	v_mfma_f32_32x32x16_f16 v[18:33], v[110:113], v[134:137], v[18:33]
	s_waitcnt lgkmcnt(0)
	v_mfma_f32_32x32x16_f16 v[2:17], v[138:141], v[134:137], v[2:17]
	v_mfma_f32_32x32x16_f16 v[34:49], v[138:141], v[114:117], v[34:49]
	ds_read_b128 v[110:113], v99
	ds_read_b128 v[114:117], v142
	ds_read_b128 v[142:145], v142 offset:4096
	ds_read_b128 v[146:149], v146 offset:4096
	s_waitcnt lgkmcnt(0)
	s_barrier
	s_waitcnt lgkmcnt(2)
	v_mfma_f32_32x32x16_f16 v[50:65], v[110:113], v[114:117], v[50:65]
	s_nop 11
	ds_write_b128 v100, v[50:53]
	ds_write_b128 v101, v[54:57]
	s_waitcnt lgkmcnt(3)
	v_mfma_f32_32x32x16_f16 v[18:33], v[110:113], v[142:145], v[18:33]
	s_waitcnt lgkmcnt(2)
	v_mfma_f32_32x32x16_f16 v[2:17], v[146:149], v[142:145], v[2:17]
	v_mfma_f32_32x32x16_f16 v[34:49], v[146:149], v[114:117], v[34:49]
	ds_write_b128 v102, v[58:61]
	ds_write_b128 v103, v[62:65]
	s_nop 9
	ds_write_b128 v104, v[34:37]
	ds_write_b128 v105, v[38:41]
	ds_write_b128 v106, v[42:45]
	ds_write_b128 v107, v[46:49]
	ds_write_b128 v100, v[18:21] offset:16384
	ds_write_b128 v101, v[22:25] offset:16384
	ds_write_b128 v102, v[26:29] offset:16384
	ds_write_b128 v103, v[30:33] offset:16384
	ds_write_b128 v104, v[2:5] offset:16384
	ds_write_b128 v105, v[6:9] offset:16384
	ds_write_b128 v106, v[10:13] offset:16384
	ds_write_b128 v107, v[14:17] offset:16384
	v_or_b32_e32 v25, s14, v1
	v_lshl_add_u64 v[22:23], s[2:3], 1, v[70:71]
	s_waitcnt lgkmcnt(0)
	s_barrier
	v_mad_i64_i32 v[2:3], s[0:1], v25, s29, v[22:23]
	v_mov_b64_e32 v[10:11], v[160:161]
	v_mov_b64_e32 v[12:13], v[162:163]
	v_lshl_add_u64 v[14:15], s[2:3], 2, v[68:69]
	v_mov_b64_e32 v[6:7], v[176:177]
	v_mov_b64_e32 v[8:9], v[178:179]
	v_mov_b64_e32 v[2:3], v[180:181]
	v_mov_b64_e32 v[4:5], v[182:183]
	v_add_u32_e32 v14, 0, v85
	v_add_u32_e32 v18, s28, v85
	ds_read_b128 v[14:17], v14
	ds_read_b128 v[26:29], v18
	v_or_b32_e32 v18, 32, v25
	v_mad_i64_i32 v[18:19], s[0:1], v18, s29, v[22:23]
	v_mov_b64_e32 v[18:19], v[164:165]
	v_mov_b64_e32 v[20:21], v[166:167]
	s_waitcnt lgkmcnt(0)
	v_pk_add_f32 v[16:17], v[16:17], v[28:29]
	v_add_f32_e32 v35, v14, v26
	v_mov_b32_e32 v34, v27
	v_xor_b32_e32 v24, 8, v108
	v_cvt_f32_f16_e32 v30, v11
	v_cvt_f32_f16_sdwa v31, v11 dst_sel:DWORD dst_unused:UNUSED_PAD src0_sel:WORD_1
	v_add_u32_e32 v11, 0, v86
	v_pk_add_f32 v[16:17], v[8:9], v[16:17]
	ds_read_b128 v[26:29], v11
	v_add_u32_e32 v11, s28, v86
	v_pk_add_f32 v[36:37], v[16:17], v[30:31]
	ds_read_b128 v[30:33], v11
	v_cvt_f32_f16_e32 v38, v13
	v_cvt_f32_f16_sdwa v39, v13 dst_sel:DWORD dst_unused:UNUSED_PAD src0_sel:WORD_1
	v_mov_b32_e32 v16, v2
	v_mov_b32_e32 v17, v3
	s_waitcnt lgkmcnt(0)
	v_pk_add_f32 v[28:29], v[28:29], v[32:33]
	v_cvt_f32_f16_e32 v32, v10
	v_pk_add_f32 v[28:29], v[4:5], v[28:29]
	v_pk_mov_b32 v[16:17], v[26:27], v[16:17] op_sel:[1,0]
	v_pk_add_f32 v[28:29], v[28:29], v[38:39]
	v_cvt_f32_f16_e32 v38, v12
	v_add_f32_e32 v26, v26, v30
	v_cvt_f32_f16_sdwa v33, v10 dst_sel:DWORD dst_unused:UNUSED_PAD src0_sel:WORD_1
	v_cvt_f32_f16_sdwa v30, v12 dst_sel:DWORD dst_unused:UNUSED_PAD src0_sel:WORD_1
	v_or_b32_e32 v12, 64, v25
	v_pk_mov_b32 v[14:15], v[14:15], v[6:7] op_sel:[1,0]
	v_mad_i64_i32 v[40:41], s[0:1], v12, s29, v[22:23]
	v_or_b32_e32 v12, 0x60, v25
	v_mov_b32_e32 v10, v31
	v_mov_b32_e32 v11, v26
	v_mad_i64_i32 v[42:43], s[0:1], v12, s29, v[22:23]
	v_pk_add_f32 v[44:45], v[14:15], v[34:35]
	v_mov_b32_e32 v12, v7
	v_mov_b32_e32 v13, v32
	v_pk_add_f32 v[10:11], v[16:17], v[10:11]
	v_pk_add_f32 v[46:47], v[12:13], v[44:45]
	v_mov_b32_e32 v22, v3
	v_mov_b32_e32 v23, v38
	v_pk_add_f32 v[48:49], v[22:23], v[10:11]
	v_mov_b32_e32 v10, v33
	v_mov_b32_e32 v11, v47
	v_pk_add_f32 v[50:51], v[46:47], v[10:11]
	v_mov_b64_e32 v[14:15], v[168:169]
	v_mov_b64_e32 v[16:17], v[170:171]
	v_mov_b64_e32 v[10:11], v[172:173]
	v_mov_b64_e32 v[12:13], v[174:175]
	v_mov_b32_e32 v31, v49
	v_pk_add_f32 v[40:41], v[48:49], v[30:31]
	v_pk_mov_b32 v[30:31], v[34:35], v[44:45] op_sel:[1,0]
	v_mov_b32_e32 v27, v44
	v_mov_b32_e32 v3, v7
	v_pk_add_f32 v[30:31], v[6:7], v[30:31]
	v_mov_b32_e32 v39, v33
	v_pk_add_f32 v[26:27], v[2:3], v[26:27]
	v_pk_add_f32 v[30:31], v[30:31], v[32:33]
	v_pk_add_f32 v[26:27], v[26:27], v[38:39]
	v_pk_mul_f32 v[32:33], v[46:47], v[46:47]
	v_pk_add_f32 v[34:35], v[30:31], v[26:27]
	v_pk_mul_f32 v[26:27], v[30:31], v[26:27]
	v_mov_b32_e32 v51, v33
	v_pk_mul_f32 v[32:33], v[48:49], v[48:49]
	v_mov_b32_e32 v35, v27
	v_pk_mul_f32 v[26:27], v[40:41], v[40:41]
	v_mov_b32_e32 v32, v40
	v_mov_b32_e32 v67, v26
	v_pk_add_f32 v[32:33], v[50:51], v[32:33]
	v_pk_add_f32 v[26:27], v[34:35], v[66:67]
	v_pk_mul_f32 v[30:31], v[36:37], v[36:37]
	v_pk_mul_f32 v[34:35], v[28:29], v[28:29]
	v_and_b32_e32 v23, 64, v108
	v_pk_add_f32 v[26:27], v[32:33], v[26:27]
	v_mov_b32_e32 v32, v36
	v_mov_b32_e32 v33, v30
	v_mov_b32_e32 v38, v28
	v_mov_b32_e32 v39, v34
	v_add_u32_e32 v23, 64, v23
	v_pk_add_f32 v[32:33], v[32:33], v[38:39]
	v_mov_b32_e32 v30, v37
	v_mov_b32_e32 v34, v29
	v_cmp_lt_i32_e64 s[0:1], v24, v23
	v_pk_add_f32 v[26:27], v[26:27], v[32:33]
	v_pk_add_f32 v[30:31], v[30:31], v[34:35]
	v_cndmask_b32_e64 v24, v108, v24, s[0:1]
	v_pk_add_f32 v[26:27], v[26:27], v[30:31]
	v_lshlrev_b32_e32 v30, 2, v24
	s_nop 1
	v_mov_b32_dpp v32, v26 row_mirror row_mask:0xf bank_mask:0xf
	v_mov_b32_dpp v33, v27 row_mirror row_mask:0xf bank_mask:0xf
	v_xor_b32_e32 v24, 4, v108
	v_cmp_lt_i32_e64 s[0:1], v24, v23
	v_cvt_pk_f16_f32 v39, v28, v29
	v_or_b32_e32 v31, s2, v78
	v_cndmask_b32_e64 v24, v108, v24, s[0:1]
	s_waitcnt lgkmcnt(0)
	v_pk_add_f32 v[26:27], v[26:27], v[32:33]
	v_lshlrev_b32_e32 v32, 2, v24
	s_nop 1
	v_mov_b32_dpp v34, v26 row_half_mirror row_mask:0xf bank_mask:0xf
	v_mov_b32_dpp v35, v27 row_half_mirror row_mask:0xf bank_mask:0xf
	v_xor_b32_e32 v24, 2, v108
	v_cmp_lt_i32_e64 s[0:1], v24, v23
	v_cvt_pk_f16_f32 v37, v36, v37
	v_cvt_pk_f16_f32 v36, v47, v50
	v_cndmask_b32_e64 v24, v108, v24, s[0:1]
	s_waitcnt lgkmcnt(0)
	v_pk_add_f32 v[26:27], v[26:27], v[34:35]
	v_lshlrev_b32_e32 v33, 2, v24
	s_nop 1
	v_mov_b32_dpp v28, v26 quad_perm:[2,3,0,1] row_mask:0xf bank_mask:0xf
	v_mov_b32_dpp v29, v27 quad_perm:[2,3,0,1] row_mask:0xf bank_mask:0xf
	v_mul_lo_u32 v24, v25, s30
	v_add_lshl_u32 v24, v31, v24, 1
	v_cvt_pk_f16_f32 v38, v49, v40
	buffer_store_dwordx4 v[36:39], v24, s[8:11], 0 offen sc1
	s_waitcnt lgkmcnt(0)
	v_pk_add_f32 v[26:27], v[26:27], v[28:29]
	v_xor_b32_e32 v28, 1, v108
	v_cmp_lt_i32_e64 s[0:1], v28, v23
	s_lshl_b32 s2, s15, 4
	v_mov_b32_e32 v24, v7
	v_cndmask_b32_e64 v23, v108, v28, s[0:1]
	v_lshlrev_b32_e32 v34, 2, v23
	s_nop 1
	v_mov_b32_dpp v28, v26 quad_perm:[1,0,3,2] row_mask:0xf bank_mask:0xf
	v_mov_b32_dpp v29, v27 quad_perm:[1,0,3,2] row_mask:0xf bank_mask:0xf
	s_and_saveexec_b64 s[0:1], vcc
	s_cbranch_execz .LBB7_5
	s_waitcnt lgkmcnt(0)
	v_pk_add_f32 v[64:65], v[26:27], v[28:29]
	v_lshl_add_u32 v23, v25, 6, s2
	v_mov_b32_e32 v67, v66
	s_mov_b32 s18, s10
	s_mov_b32 s19, s11
	buffer_store_dwordx4 v[64:67], v23, s[16:19], 0 offen sc1
.LBB7_5:
	s_or_b64 exec, exec, s[0:1]
	v_add_u32_e32 v23, 0, v88
	v_add_u32_e32 v25, s28, v88
	s_waitcnt lgkmcnt(0)
	ds_read_b128 v[26:29], v23
	ds_read_b128 v[36:39], v25
	v_add_u32_e32 v23, 0, v89
	v_add_u32_e32 v25, s28, v89
	ds_read_b128 v[40:43], v23
	ds_read_b128 v[44:47], v25
	v_cvt_f32_f16_e32 v50, v18
	s_waitcnt lgkmcnt(2)
	v_add_f32_e32 v49, v26, v36
	v_cvt_f32_f16_sdwa v51, v18 dst_sel:DWORD dst_unused:UNUSED_PAD src0_sel:WORD_1
	v_cvt_f32_f16_sdwa v55, v19 dst_sel:DWORD dst_unused:UNUSED_PAD src0_sel:WORD_1
	v_cvt_f32_f16_e32 v54, v19
	v_pk_mov_b32 v[26:27], v[26:27], v[6:7] op_sel:[1,0]
	v_mov_b32_e32 v48, v37
	v_cvt_f32_f16_e32 v52, v20
	v_pk_add_f32 v[26:27], v[26:27], v[48:49]
	v_pk_add_f32 v[28:29], v[28:29], v[38:39]
	v_pk_mov_b32 v[36:37], v[48:49], v[26:27] op_sel:[1,0]
	s_waitcnt lgkmcnt(0)
	v_add_f32_e32 v18, v40, v44
	v_pk_add_f32 v[28:29], v[8:9], v[28:29]
	v_pk_add_f32 v[36:37], v[6:7], v[36:37]
	v_mov_b32_e32 v25, v50
	v_cvt_f32_f16_sdwa v20, v20 dst_sel:DWORD dst_unused:UNUSED_PAD src0_sel:WORD_1
	v_pk_add_f32 v[28:29], v[28:29], v[54:55]
	v_mov_b32_e32 v19, v26
	v_pk_add_f32 v[54:55], v[24:25], v[26:27]
	v_pk_add_f32 v[26:27], v[36:37], v[50:51]
	v_pk_mov_b32 v[36:37], v[40:41], v[2:3] op_sel:[1,0]
	v_mov_b32_e32 v40, v45
	v_mov_b32_e32 v41, v18
	v_pk_add_f32 v[48:49], v[2:3], v[18:19]
	v_pk_add_f32 v[18:19], v[36:37], v[40:41]
	v_mov_b32_e32 v23, v52
	v_mov_b32_e32 v53, v51
	v_cvt_f32_f16_sdwa v57, v21 dst_sel:DWORD dst_unused:UNUSED_PAD src0_sel:WORD_1
	v_cvt_f32_f16_e32 v56, v21
	v_pk_add_f32 v[40:41], v[22:23], v[18:19]
	v_pk_add_f32 v[36:37], v[48:49], v[52:53]
	v_mov_b32_e32 v18, v51
	v_mov_b32_e32 v19, v55
	v_mov_b32_e32 v21, v41
	v_pk_add_f32 v[42:43], v[42:43], v[46:47]
	v_pk_add_f32 v[44:45], v[54:55], v[18:19]
	v_pk_mul_f32 v[18:19], v[54:55], v[54:55]
	v_pk_add_f32 v[48:49], v[40:41], v[20:21]
	v_pk_add_f32 v[20:21], v[26:27], v[36:37]
	v_pk_mul_f32 v[26:27], v[26:27], v[36:37]
	v_pk_add_f32 v[42:43], v[4:5], v[42:43]
	v_mov_b32_e32 v45, v19
	v_pk_mul_f32 v[18:19], v[40:41], v[40:41]
	v_mov_b32_e32 v21, v27
	v_pk_mul_f32 v[26:27], v[48:49], v[48:49]
	v_pk_add_f32 v[42:43], v[42:43], v[56:57]
	v_mov_b32_e32 v18, v48
	v_mov_b32_e32 v67, v26
	v_pk_mul_f32 v[38:39], v[28:29], v[28:29]
	v_pk_mul_f32 v[46:47], v[42:43], v[42:43]
	v_pk_add_f32 v[18:19], v[44:45], v[18:19]
	v_pk_add_f32 v[20:21], v[20:21], v[66:67]
	v_mov_b32_e32 v26, v42
	v_pk_add_f32 v[18:19], v[18:19], v[20:21]
	v_mov_b32_e32 v20, v28
	v_mov_b32_e32 v21, v38
	v_mov_b32_e32 v27, v46
	v_pk_add_f32 v[20:21], v[20:21], v[26:27]
	v_mov_b32_e32 v38, v29
	v_mov_b32_e32 v46, v43
	v_pk_add_f32 v[18:19], v[18:19], v[20:21]
	v_pk_add_f32 v[20:21], v[38:39], v[46:47]
	v_or_b32_e32 v23, s14, v87
	v_pk_add_f32 v[18:19], v[18:19], v[20:21]
	s_nop 1
	v_mov_b32_dpp v20, v18 row_mirror row_mask:0xf bank_mask:0xf
	v_mov_b32_dpp v21, v19 row_mirror row_mask:0xf bank_mask:0xf
	v_mul_lo_u32 v25, v23, s30
	v_cvt_pk_f16_f32 v27, v28, v29
	v_cvt_pk_f16_f32 v29, v42, v43
	v_add_lshl_u32 v25, v31, v25, 1
	s_waitcnt lgkmcnt(0)
	v_pk_add_f32 v[18:19], v[18:19], v[20:21]
	s_nop 1
	v_mov_b32_dpp v20, v18 row_half_mirror row_mask:0xf bank_mask:0xf
	v_mov_b32_dpp v21, v19 row_half_mirror row_mask:0xf bank_mask:0xf
	v_cvt_pk_f16_f32 v26, v55, v44
	v_cvt_pk_f16_f32 v28, v41, v48
	buffer_store_dwordx4 v[26:29], v25, s[8:11], 0 offen sc1
	s_waitcnt lgkmcnt(0)
	v_pk_add_f32 v[18:19], v[18:19], v[20:21]
	s_nop 1
	v_mov_b32_dpp v20, v18 quad_perm:[2,3,0,1] row_mask:0xf bank_mask:0xf
	v_mov_b32_dpp v21, v19 quad_perm:[2,3,0,1] row_mask:0xf bank_mask:0xf
	s_waitcnt lgkmcnt(0)
	v_pk_add_f32 v[18:19], v[18:19], v[20:21]
	s_nop 1
	v_mov_b32_dpp v20, v18 quad_perm:[1,0,3,2] row_mask:0xf bank_mask:0xf
	v_mov_b32_dpp v21, v19 quad_perm:[1,0,3,2] row_mask:0xf bank_mask:0xf
	s_and_saveexec_b64 s[0:1], vcc
	s_cbranch_execz .LBB7_7
	s_waitcnt lgkmcnt(0)
	v_pk_add_f32 v[64:65], v[18:19], v[20:21]
	v_lshl_add_u32 v18, v23, 6, s2
	v_mov_b32_e32 v67, v66
	s_mov_b32 s18, s10
	s_mov_b32 s19, s11
	buffer_store_dwordx4 v[64:67], v18, s[16:19], 0 offen sc1
.LBB7_7:
	s_or_b64 exec, exec, s[0:1]
	v_add_u32_e32 v18, 0, v91
	v_add_u32_e32 v23, s28, v91
	s_waitcnt lgkmcnt(0)
	ds_read_b128 v[18:21], v18
	ds_read_b128 v[26:29], v23
	v_add_u32_e32 v23, 0, v92
	v_add_u32_e32 v25, s28, v92
	ds_read_b128 v[36:39], v23
	ds_read_b128 v[40:43], v25
	v_cvt_f32_f16_e32 v46, v14
	v_cvt_f32_f16_e32 v48, v16
	s_waitcnt lgkmcnt(2)
	v_add_f32_e32 v45, v18, v26
	v_cvt_f32_f16_sdwa v47, v14 dst_sel:DWORD dst_unused:UNUSED_PAD src0_sel:WORD_1
	v_pk_mov_b32 v[18:19], v[18:19], v[6:7] op_sel:[1,0]
	v_mov_b32_e32 v44, v27
	s_waitcnt lgkmcnt(0)
	v_add_f32_e32 v14, v36, v40
	v_pk_add_f32 v[18:19], v[18:19], v[44:45]
	v_cvt_f32_f16_sdwa v16, v16 dst_sel:DWORD dst_unused:UNUSED_PAD src0_sel:WORD_1
	v_cvt_f32_f16_sdwa v51, v15 dst_sel:DWORD dst_unused:UNUSED_PAD src0_sel:WORD_1
	v_cvt_f32_f16_e32 v50, v15
	v_mov_b32_e32 v15, v18
	v_pk_mov_b32 v[36:37], v[36:37], v[2:3] op_sel:[1,0]
	v_mov_b32_e32 v40, v41
	v_mov_b32_e32 v41, v14
	v_pk_mov_b32 v[26:27], v[44:45], v[18:19] op_sel:[1,0]
	v_pk_add_f32 v[44:45], v[2:3], v[14:15]
	v_mov_b32_e32 v25, v46
	v_pk_add_f32 v[14:15], v[36:37], v[40:41]
	v_mov_b32_e32 v23, v48
	v_mov_b32_e32 v49, v47
	v_cvt_f32_f16_sdwa v53, v17 dst_sel:DWORD dst_unused:UNUSED_PAD src0_sel:WORD_1
	v_cvt_f32_f16_e32 v52, v17
	v_pk_add_f32 v[26:27], v[6:7], v[26:27]
	v_pk_add_f32 v[18:19], v[24:25], v[18:19]
	v_pk_add_f32 v[40:41], v[22:23], v[14:15]
	v_pk_add_f32 v[26:27], v[26:27], v[46:47]
	v_pk_add_f32 v[36:37], v[44:45], v[48:49]
	v_mov_b32_e32 v14, v47
	v_mov_b32_e32 v15, v19
	v_mov_b32_e32 v17, v41
	v_pk_add_f32 v[20:21], v[20:21], v[28:29]
	v_pk_add_f32 v[38:39], v[38:39], v[42:43]
	v_pk_add_f32 v[44:45], v[18:19], v[14:15]
	v_pk_mul_f32 v[14:15], v[18:19], v[18:19]
	v_pk_add_f32 v[46:47], v[40:41], v[16:17]
	v_pk_add_f32 v[16:17], v[26:27], v[36:37]
	v_pk_mul_f32 v[26:27], v[26:27], v[36:37]
	v_pk_add_f32 v[20:21], v[8:9], v[20:21]
	v_pk_add_f32 v[38:39], v[4:5], v[38:39]
	v_mov_b32_e32 v45, v15
	v_pk_mul_f32 v[14:15], v[40:41], v[40:41]
	v_mov_b32_e32 v17, v27
	v_pk_mul_f32 v[26:27], v[46:47], v[46:47]
	v_pk_add_f32 v[20:21], v[20:21], v[50:51]
	v_pk_add_f32 v[38:39], v[38:39], v[52:53]
	v_mov_b32_e32 v14, v46
	v_mov_b32_e32 v67, v26
	v_pk_mul_f32 v[28:29], v[20:21], v[20:21]
	v_pk_mul_f32 v[42:43], v[38:39], v[38:39]
	v_pk_add_f32 v[14:15], v[44:45], v[14:15]
	v_pk_add_f32 v[16:17], v[16:17], v[66:67]
	v_mov_b32_e32 v26, v38
	v_pk_add_f32 v[14:15], v[14:15], v[16:17]
	v_mov_b32_e32 v16, v20
	v_mov_b32_e32 v17, v28
	v_mov_b32_e32 v27, v42
	v_pk_add_f32 v[16:17], v[16:17], v[26:27]
	v_mov_b32_e32 v28, v21
	v_mov_b32_e32 v42, v39
	v_pk_add_f32 v[14:15], v[14:15], v[16:17]
	v_pk_add_f32 v[16:17], v[28:29], v[42:43]
	v_or_b32_e32 v18, s14, v90
	v_pk_add_f32 v[14:15], v[14:15], v[16:17]
	s_nop 1
	v_mov_b32_dpp v16, v14 row_mirror row_mask:0xf bank_mask:0xf
	v_mov_b32_dpp v17, v15 row_mirror row_mask:0xf bank_mask:0xf
	v_cvt_pk_f16_f32 v27, v20, v21
	v_mul_lo_u32 v20, v18, s30
	v_cvt_pk_f16_f32 v29, v38, v39
	v_add_lshl_u32 v20, v31, v20, 1
	s_waitcnt lgkmcnt(0)
	v_pk_add_f32 v[14:15], v[14:15], v[16:17]
	s_nop 1
	v_mov_b32_dpp v16, v14 row_half_mirror row_mask:0xf bank_mask:0xf
	v_mov_b32_dpp v17, v15 row_half_mirror row_mask:0xf bank_mask:0xf
	v_cvt_pk_f16_f32 v26, v19, v44
	v_cvt_pk_f16_f32 v28, v41, v46
	buffer_store_dwordx4 v[26:29], v20, s[8:11], 0 offen sc1
	s_waitcnt lgkmcnt(0)
	v_pk_add_f32 v[14:15], v[14:15], v[16:17]
	s_nop 1
	v_mov_b32_dpp v16, v14 quad_perm:[2,3,0,1] row_mask:0xf bank_mask:0xf
	v_mov_b32_dpp v17, v15 quad_perm:[2,3,0,1] row_mask:0xf bank_mask:0xf
	s_waitcnt lgkmcnt(0)
	v_pk_add_f32 v[14:15], v[14:15], v[16:17]
	s_nop 1
	v_mov_b32_dpp v16, v14 quad_perm:[1,0,3,2] row_mask:0xf bank_mask:0xf
	v_mov_b32_dpp v17, v15 quad_perm:[1,0,3,2] row_mask:0xf bank_mask:0xf
	s_and_saveexec_b64 s[0:1], vcc
	s_cbranch_execz .LBB7_9
	s_waitcnt lgkmcnt(0)
	v_pk_add_f32 v[64:65], v[14:15], v[16:17]
	v_lshl_add_u32 v14, v18, 6, s2
	v_mov_b32_e32 v67, v66
	s_mov_b32 s18, s10
	s_mov_b32 s19, s11
	buffer_store_dwordx4 v[64:67], v14, s[16:19], 0 offen sc1
.LBB7_9:
	s_or_b64 exec, exec, s[0:1]
	v_add_u32_e32 v14, 0, v94
	v_add_u32_e32 v18, s28, v94
	s_waitcnt lgkmcnt(0)
	ds_read_b128 v[14:17], v14
	ds_read_b128 v[18:21], v18
	v_add_u32_e32 v23, 0, v95
	v_add_u32_e32 v25, s28, v95
	ds_read_b128 v[26:29], v23
	ds_read_b128 v[36:39], v25
	v_cvt_f32_f16_e32 v42, v10
	s_waitcnt lgkmcnt(2)
	v_add_f32_e32 v41, v14, v18
	v_cvt_f32_f16_sdwa v43, v10 dst_sel:DWORD dst_unused:UNUSED_PAD src0_sel:WORD_1
	v_cvt_f32_f16_e32 v44, v12
	v_pk_mov_b32 v[14:15], v[14:15], v[6:7] op_sel:[1,0]
	v_mov_b32_e32 v40, v19
	v_pk_add_f32 v[14:15], v[14:15], v[40:41]
	s_waitcnt lgkmcnt(0)
	v_add_f32_e32 v10, v26, v36
	v_cvt_f32_f16_sdwa v47, v11 dst_sel:DWORD dst_unused:UNUSED_PAD src0_sel:WORD_1
	v_cvt_f32_f16_e32 v46, v11
	v_pk_mov_b32 v[18:19], v[40:41], v[14:15] op_sel:[1,0]
	v_mov_b32_e32 v11, v14
	v_mov_b32_e32 v25, v42
	v_cvt_f32_f16_sdwa v12, v12 dst_sel:DWORD dst_unused:UNUSED_PAD src0_sel:WORD_1
	v_pk_add_f32 v[6:7], v[6:7], v[18:19]
	v_pk_add_f32 v[18:19], v[2:3], v[10:11]
	v_pk_add_f32 v[14:15], v[24:25], v[14:15]
	v_pk_mov_b32 v[2:3], v[26:27], v[2:3] op_sel:[1,0]
	v_mov_b32_e32 v24, v37
	v_mov_b32_e32 v25, v10
	v_mov_b32_e32 v45, v43
	v_pk_add_f32 v[2:3], v[2:3], v[24:25]
	v_mov_b32_e32 v23, v44
	v_cvt_f32_f16_sdwa v49, v13 dst_sel:DWORD dst_unused:UNUSED_PAD src0_sel:WORD_1
	v_cvt_f32_f16_e32 v48, v13
	v_pk_add_f32 v[10:11], v[18:19], v[44:45]
	v_pk_add_f32 v[18:19], v[22:23], v[2:3]
	v_pk_add_f32 v[6:7], v[6:7], v[42:43]
	v_mov_b32_e32 v2, v43
	v_mov_b32_e32 v3, v15
	v_mov_b32_e32 v13, v19
	v_pk_add_f32 v[16:17], v[16:17], v[20:21]
	v_pk_add_f32 v[20:21], v[28:29], v[38:39]
	v_pk_add_f32 v[22:23], v[14:15], v[2:3]
	v_pk_mul_f32 v[2:3], v[14:15], v[14:15]
	v_pk_add_f32 v[12:13], v[18:19], v[12:13]
	v_pk_add_f32 v[24:25], v[6:7], v[10:11]
	v_pk_mul_f32 v[6:7], v[6:7], v[10:11]
	v_pk_add_f32 v[8:9], v[8:9], v[16:17]
	v_pk_add_f32 v[4:5], v[4:5], v[20:21]
	v_mov_b32_e32 v23, v3
	v_pk_mul_f32 v[2:3], v[18:19], v[18:19]
	v_mov_b32_e32 v25, v7
	v_pk_mul_f32 v[6:7], v[12:13], v[12:13]
	v_pk_add_f32 v[8:9], v[8:9], v[46:47]
	v_pk_add_f32 v[4:5], v[4:5], v[48:49]
	v_mov_b32_e32 v2, v12
	v_mov_b32_e32 v67, v6
	v_pk_mul_f32 v[16:17], v[8:9], v[8:9]
	v_pk_mul_f32 v[20:21], v[4:5], v[4:5]
	v_pk_add_f32 v[2:3], v[22:23], v[2:3]
	v_pk_add_f32 v[6:7], v[24:25], v[66:67]
	v_mov_b32_e32 v10, v4
	v_pk_add_f32 v[2:3], v[2:3], v[6:7]
	v_mov_b32_e32 v6, v8
	v_mov_b32_e32 v7, v16
	v_mov_b32_e32 v11, v20
	v_pk_add_f32 v[6:7], v[6:7], v[10:11]
	v_mov_b32_e32 v16, v9
	v_mov_b32_e32 v20, v5
	v_pk_add_f32 v[2:3], v[2:3], v[6:7]
	v_pk_add_f32 v[6:7], v[16:17], v[20:21]
	v_cvt_pk_f16_f32 v11, v4, v5
	v_pk_add_f32 v[2:3], v[2:3], v[6:7]
	s_nop 1
	v_mov_b32_dpp v6, v2 row_mirror row_mask:0xf bank_mask:0xf
	v_mov_b32_dpp v7, v3 row_mirror row_mask:0xf bank_mask:0xf
	v_cvt_pk_f16_f32 v9, v8, v9
	v_cvt_pk_f16_f32 v8, v15, v22
	v_cvt_pk_f16_f32 v10, v19, v12
	s_waitcnt lgkmcnt(0)
	v_pk_add_f32 v[2:3], v[2:3], v[6:7]
	s_nop 1
	v_mov_b32_dpp v6, v2 row_half_mirror row_mask:0xf bank_mask:0xf
	v_mov_b32_dpp v7, v3 row_half_mirror row_mask:0xf bank_mask:0xf
	s_waitcnt lgkmcnt(0)
	v_pk_add_f32 v[2:3], v[2:3], v[6:7]
	s_nop 1
	v_mov_b32_dpp v16, v2 quad_perm:[2,3,0,1] row_mask:0xf bank_mask:0xf
	v_mov_b32_dpp v17, v3 quad_perm:[2,3,0,1] row_mask:0xf bank_mask:0xf
	v_add_u32_e32 v6, s14, v93
	v_mul_lo_u32 v7, v6, s30
	v_add_lshl_u32 v7, v31, v7, 1
	buffer_store_dwordx4 v[8:11], v7, s[8:11], 0 offen sc1
	s_waitcnt lgkmcnt(0)
	v_pk_add_f32 v[2:3], v[2:3], v[16:17]
	s_nop 1
	v_mov_b32_dpp v4, v2 quad_perm:[1,0,3,2] row_mask:0xf bank_mask:0xf
	v_mov_b32_dpp v5, v3 quad_perm:[1,0,3,2] row_mask:0xf bank_mask:0xf
	s_and_saveexec_b64 s[0:1], vcc
	s_cbranch_execz .LBB7_2
	s_waitcnt lgkmcnt(0)
	v_pk_add_f32 v[64:65], v[2:3], v[4:5]
	v_lshl_add_u32 v2, v6, 6, s2
	v_mov_b32_e32 v67, v66
	s_mov_b32 s18, s10
	s_mov_b32 s19, s11
	buffer_store_dwordx4 v[64:67], v2, s[16:19], 0 offen sc1
	s_branch .LBB7_2

.LBB9_3:
	s_ashr_i32 s44, s23, 31
	s_xor_b32 s44, s44, s25
	s_abs_i32 s45, s23
	s_mul_hi_u32 s48, s45, s26
	s_mul_i32 s49, s48, s24
	s_sub_i32 s45, s45, s49
	s_add_i32 s49, s48, 1
	s_sub_i32 s46, s45, s24
	s_cmp_ge_u32 s45, s24
	s_cselect_b32 s48, s49, s48
	s_cselect_b32 s45, s46, s45
	s_add_i32 s49, s48, 1
	s_cmp_ge_u32 s45, s24
	s_cselect_b32 s45, s49, s48
	s_xor_b32 s45, s45, s44
	s_sub_i32 s44, s45, s44
	s_mul_i32 s45, s44, s21
	s_sub_i32 s47, s23, s45
	s_lshl_b32 s48, s47, 7
	s_lshl_b32 s46, s44, 7
	s_ashr_i32 s49, s48, 31
	v_or_b32_e32 v152, s46, v1
	v_lshl_add_u64 v[154:155], s[48:49], 1, v[70:71]
	v_mad_i64_i32 v[156:157], s[50:51], v152, s29, v[154:155]
	v_lshl_add_u64 v[158:159], s[48:49], 2, v[68:69]
	v_or_b32_e32 v153, 32, v152
	global_load_dwordx4 v[160:163], v[156:157], off
	v_mad_i64_i32 v[184:185], s[50:51], v153, s29, v[154:155]
	v_or_b32_e32 v153, 64, v152
	global_load_dwordx4 v[176:179], v[158:159], off
	global_load_dwordx4 v[180:183], v[158:159], off offset:16
	v_mad_i64_i32 v[186:187], s[50:51], v153, s29, v[154:155]
	v_or_b32_e32 v153, 0x60, v152
	global_load_dwordx4 v[164:167], v[184:185], off
	v_mad_i64_i32 v[188:189], s[50:51], v153, s29, v[154:155]
	global_load_dwordx4 v[168:171], v[186:187], off
	s_nop 0
	global_load_dwordx4 v[172:175], v[188:189], off
	v_add_u32_e32 v110, v80, v76
	s_waitcnt vmcnt(14)
	s_barrier
	s_waitcnt lgkmcnt(0)
	ds_read_b128 v[2:5], v110 offset:16384
	v_add_u32_e32 v111, v79, v76
	ds_read_b128 v[6:9], v111
	ds_read_b128 v[10:13], v111 offset:4096
	ds_read_b128 v[14:17], v110 offset:20480
	v_add_u32_e32 v67, v80, v77
	ds_read_b128 v[34:37], v67 offset:16384
	v_add_u32_e32 v109, v79, v77
	s_waitcnt lgkmcnt(3)
	v_mfma_f32_32x32x16_f16 v[50:65], v[2:5], v[6:9], 0
	ds_read_b128 v[112:115], v109
	ds_read_b128 v[116:119], v109 offset:4096
	ds_read_b128 v[120:123], v67 offset:20480
	v_readfirstlane_b32 s2, v0
	s_lshl_b32 s35, s27, 15
	s_lshl_b32 s2, s2, 4
	s_add_i32 s1, s35, 0
	s_and_b32 s39, s2, 0xfffffc00
	s_add_i32 s1, s1, s39
	s_waitcnt lgkmcnt(5)
	v_mfma_f32_32x32x16_f16 v[18:33], v[2:5], v[10:13], 0
	s_mov_b32 m0, s1
	s_add_i32 s2, s1, 0x2000
	buffer_load_dwordx4 v72, s[4:7], s0 offen lds
	s_mov_b32 m0, s2
	s_add_i32 s3, s1, 0x4000
	buffer_load_dwordx4 v74, s[4:7], s0 offen lds
	s_mov_b32 s14, s10
	s_waitcnt lgkmcnt(2)
	v_mfma_f32_32x32x16_f16 v[50:65], v[34:37], v[112:115], v[50:65]
	s_mov_b32 s15, s11
	s_mov_b32 m0, s3
	s_add_i32 s18, s1, 0x6000
	buffer_load_dwordx4 v73, s[12:15], s0 offen lds
	s_mov_b32 m0, s18
	s_add_i32 s19, s35, 0x8000
	buffer_load_dwordx4 v75, s[12:15], s0 offen lds
	s_waitcnt lgkmcnt(1)
	v_mfma_f32_32x32x16_f16 v[18:33], v[34:37], v[116:119], v[18:33]
	s_waitcnt vmcnt(14)
	s_barrier
	s_and_b32 s19, s19, 0x18000
	s_add_i32 s19, s19, 0
	s_add_i32 s19, s19, s39
	s_add_i32 s36, s0, 0x80
	s_mov_b32 m0, s19
	v_mfma_f32_32x32x16_f16 v[34:49], v[14:17], v[6:9], 0
	s_add_i32 s31, s19, 0x2000
	s_add_i32 s33, s19, 0x4000
	s_add_i32 s34, s19, 0x6000
	s_xor_b32 s40, s35, 0x10000
	s_add_i32 s35, s40, 0
	s_add_i32 s35, s35, s39
	s_add_i32 s41, s0, 0x100
	v_mfma_f32_32x32x16_f16 v[2:17], v[14:17], v[10:13], 0
	s_add_i32 s37, s35, 0x4000
	s_add_i32 s38, s35, 0x6000
	s_add_i32 s40, s40, 0x8000
	s_and_b32 s40, s40, 0x18000
	s_add_i32 s40, s40, 0
	s_add_i32 s39, s40, s39
	s_add_i32 s43, s0, 0x180
	s_waitcnt lgkmcnt(0)
	v_mfma_f32_32x32x16_f16 v[34:49], v[120:123], v[112:115], v[34:49]
	s_add_i32 s40, s39, 0x2000
	s_add_i32 s42, s39, 0x6000
	v_mfma_f32_32x32x16_f16 v[2:17], v[120:123], v[116:119], v[2:17]
	ds_read_b128 v[112:115], v110 offset:49152
	ds_read_b128 v[116:119], v111 offset:32768
	ds_read_b128 v[120:123], v111 offset:36864
	ds_read_b128 v[124:127], v110 offset:53248
	s_waitcnt lgkmcnt(2)
	v_mfma_f32_32x32x16_f16 v[50:65], v[112:115], v[116:119], v[50:65]
	s_waitcnt lgkmcnt(1)
	v_mfma_f32_32x32x16_f16 v[18:33], v[112:115], v[120:123], v[18:33]
	s_waitcnt lgkmcnt(0)
	v_mfma_f32_32x32x16_f16 v[34:49], v[124:127], v[116:119], v[34:49]
	v_mfma_f32_32x32x16_f16 v[2:17], v[124:127], v[120:123], v[2:17]
	ds_read_b128 v[112:115], v67 offset:49152
	ds_read_b128 v[116:119], v109 offset:32768
	ds_read_b128 v[120:123], v109 offset:36864
	ds_read_b128 v[124:127], v67 offset:53248
	buffer_load_dwordx4 v72, s[4:7], s36 offen lds
	s_mov_b32 m0, s31
	s_nop 0
	buffer_load_dwordx4 v74, s[4:7], s36 offen lds
	s_mov_b32 m0, s33
	s_nop 0
	buffer_load_dwordx4 v73, s[12:15], s36 offen lds
	s_mov_b32 m0, s34
	s_waitcnt lgkmcnt(2)
	v_mfma_f32_32x32x16_f16 v[50:65], v[112:115], v[116:119], v[50:65]
	buffer_load_dwordx4 v75, s[12:15], s36 offen lds
	s_waitcnt vmcnt(14)
	s_barrier
	s_mov_b32 m0, s35
	s_add_i32 s36, s35, 0x2000
	s_waitcnt lgkmcnt(1)
	v_mfma_f32_32x32x16_f16 v[18:33], v[112:115], v[120:123], v[18:33]
	v_add_u32_e32 v113, v81, v76
	v_add_u32_e32 v112, v82, v76
	s_waitcnt lgkmcnt(0)
	v_mfma_f32_32x32x16_f16 v[34:49], v[124:127], v[116:119], v[34:49]
	ds_read_b128 v[114:117], v96
	v_mfma_f32_32x32x16_f16 v[2:17], v[124:127], v[120:123], v[2:17]
	ds_read_b128 v[118:121], v113
	ds_read_b128 v[122:125], v113 offset:4096
	ds_read_b128 v[126:129], v112 offset:4096
	s_waitcnt lgkmcnt(2)
	v_mfma_f32_32x32x16_f16 v[50:65], v[114:117], v[118:121], v[50:65]
	s_waitcnt lgkmcnt(1)
	v_mfma_f32_32x32x16_f16 v[18:33], v[114:117], v[122:125], v[18:33]
	v_add_u32_e32 v115, v81, v77
	v_add_u32_e32 v114, v82, v77
	s_waitcnt lgkmcnt(0)
	v_mfma_f32_32x32x16_f16 v[34:49], v[126:129], v[118:121], v[34:49]
	ds_read_b128 v[116:119], v97
	v_mfma_f32_32x32x16_f16 v[2:17], v[126:129], v[122:125], v[2:17]
	ds_read_b128 v[120:123], v115
	ds_read_b128 v[124:127], v115 offset:4096
	ds_read_b128 v[128:131], v114 offset:4096
	buffer_load_dwordx4 v72, s[4:7], s41 offen lds
	s_mov_b32 m0, s36
	s_nop 0
	buffer_load_dwordx4 v74, s[4:7], s41 offen lds
	s_mov_b32 m0, s37
	s_waitcnt lgkmcnt(2)
	v_mfma_f32_32x32x16_f16 v[50:65], v[116:119], v[120:123], v[50:65]
	buffer_load_dwordx4 v73, s[12:15], s41 offen lds
	s_mov_b32 m0, s38
	s_nop 0
	buffer_load_dwordx4 v75, s[12:15], s41 offen lds
	s_waitcnt vmcnt(8)
	s_barrier
	s_mov_b32 m0, s39
	s_waitcnt lgkmcnt(1)
	v_mfma_f32_32x32x16_f16 v[18:33], v[116:119], v[124:127], v[18:33]
	v_add_u32_e32 v117, v83, v76
	v_add_u32_e32 v116, v84, v76
	s_add_i32 s41, s39, 0x4000
	s_waitcnt lgkmcnt(0)
	v_mfma_f32_32x32x16_f16 v[34:49], v[128:131], v[120:123], v[34:49]
	ds_read_b128 v[118:121], v98
	v_mfma_f32_32x32x16_f16 v[2:17], v[128:131], v[124:127], v[2:17]
	ds_read_b128 v[122:125], v117
	ds_read_b128 v[126:129], v117 offset:4096
	ds_read_b128 v[130:133], v116 offset:4096
	s_waitcnt lgkmcnt(2)
	v_mfma_f32_32x32x16_f16 v[50:65], v[118:121], v[122:125], v[50:65]
	s_waitcnt lgkmcnt(1)
	v_mfma_f32_32x32x16_f16 v[18:33], v[118:121], v[126:129], v[18:33]
	v_add_u32_e32 v119, v83, v77
	v_add_u32_e32 v118, v84, v77
	s_waitcnt lgkmcnt(0)
	v_mfma_f32_32x32x16_f16 v[34:49], v[130:133], v[122:125], v[34:49]
	ds_read_b128 v[120:123], v99
	v_mfma_f32_32x32x16_f16 v[2:17], v[130:133], v[126:129], v[2:17]
	ds_read_b128 v[124:127], v119
	ds_read_b128 v[128:131], v119 offset:4096
	ds_read_b128 v[132:135], v118 offset:4096
	buffer_load_dwordx4 v72, s[4:7], s43 offen lds
	s_mov_b32 m0, s40
	s_nop 0
	buffer_load_dwordx4 v74, s[4:7], s43 offen lds
	s_mov_b32 m0, s41
	s_waitcnt lgkmcnt(2)
	v_mfma_f32_32x32x16_f16 v[50:65], v[120:123], v[124:127], v[50:65]
	buffer_load_dwordx4 v73, s[12:15], s43 offen lds
	s_mov_b32 m0, s42
	s_nop 0
	buffer_load_dwordx4 v75, s[12:15], s43 offen lds
	s_waitcnt vmcnt(8)
	s_barrier
	s_add_i32 s43, s0, 0x200
	s_waitcnt lgkmcnt(1)
	v_mfma_f32_32x32x16_f16 v[18:33], v[120:123], v[128:131], v[18:33]
	s_mov_b32 m0, s1
	s_waitcnt lgkmcnt(0)
	v_mfma_f32_32x32x16_f16 v[34:49], v[132:135], v[124:127], v[34:49]
	v_mfma_f32_32x32x16_f16 v[2:17], v[132:135], v[128:131], v[2:17]
	ds_read_b128 v[120:123], v110 offset:16384
	ds_read_b128 v[124:127], v111
	ds_read_b128 v[128:131], v111 offset:4096
	ds_read_b128 v[132:135], v110 offset:20480
	s_waitcnt lgkmcnt(2)
	v_mfma_f32_32x32x16_f16 v[50:65], v[120:123], v[124:127], v[50:65]
	s_waitcnt lgkmcnt(1)
	v_mfma_f32_32x32x16_f16 v[18:33], v[120:123], v[128:131], v[18:33]
	s_waitcnt lgkmcnt(0)
	v_mfma_f32_32x32x16_f16 v[34:49], v[132:135], v[124:127], v[34:49]
	v_mfma_f32_32x32x16_f16 v[2:17], v[132:135], v[128:131], v[2:17]
	ds_read_b128 v[120:123], v67 offset:16384
	ds_read_b128 v[124:127], v109
	ds_read_b128 v[128:131], v109 offset:4096
	ds_read_b128 v[132:135], v67 offset:20480
	buffer_load_dwordx4 v72, s[4:7], s43 offen lds
	s_mov_b32 m0, s2
	s_nop 0
	buffer_load_dwordx4 v74, s[4:7], s43 offen lds
	s_mov_b32 m0, s3
	s_waitcnt lgkmcnt(2)
	v_mfma_f32_32x32x16_f16 v[50:65], v[120:123], v[124:127], v[50:65]
	buffer_load_dwordx4 v73, s[12:15], s43 offen lds
	s_mov_b32 m0, s18
	s_nop 0
	buffer_load_dwordx4 v75, s[12:15], s43 offen lds
	s_waitcnt vmcnt(8)
	s_barrier
	s_add_i32 s43, s0, 0x280
	s_waitcnt lgkmcnt(1)
	v_mfma_f32_32x32x16_f16 v[18:33], v[120:123], v[128:131], v[18:33]
	s_mov_b32 m0, s19
	s_waitcnt lgkmcnt(0)
	v_mfma_f32_32x32x16_f16 v[34:49], v[132:135], v[124:127], v[34:49]
	v_mfma_f32_32x32x16_f16 v[2:17], v[132:135], v[128:131], v[2:17]
	ds_read_b128 v[120:123], v110 offset:49152
	ds_read_b128 v[124:127], v111 offset:32768
	ds_read_b128 v[128:131], v111 offset:36864
	ds_read_b128 v[132:135], v110 offset:53248
	s_waitcnt lgkmcnt(2)
	v_mfma_f32_32x32x16_f16 v[50:65], v[120:123], v[124:127], v[50:65]
	s_waitcnt lgkmcnt(1)
	v_mfma_f32_32x32x16_f16 v[18:33], v[120:123], v[128:131], v[18:33]
	s_waitcnt lgkmcnt(0)
	v_mfma_f32_32x32x16_f16 v[34:49], v[132:135], v[124:127], v[34:49]
	v_mfma_f32_32x32x16_f16 v[2:17], v[132:135], v[128:131], v[2:17]
	ds_read_b128 v[120:123], v67 offset:49152
	ds_read_b128 v[124:127], v109 offset:32768
	ds_read_b128 v[128:131], v109 offset:36864
	ds_read_b128 v[132:135], v67 offset:53248
	buffer_load_dwordx4 v72, s[4:7], s43 offen lds
	s_mov_b32 m0, s31
	s_nop 0
	buffer_load_dwordx4 v74, s[4:7], s43 offen lds
	s_mov_b32 m0, s33
	s_waitcnt lgkmcnt(2)
	v_mfma_f32_32x32x16_f16 v[50:65], v[120:123], v[124:127], v[50:65]
	buffer_load_dwordx4 v73, s[12:15], s43 offen lds
	s_mov_b32 m0, s34
	s_nop 0
	buffer_load_dwordx4 v75, s[12:15], s43 offen lds
	s_waitcnt vmcnt(8)
	s_barrier
	s_add_i32 s43, s0, 0x300
	s_waitcnt lgkmcnt(1)
	v_mfma_f32_32x32x16_f16 v[18:33], v[120:123], v[128:131], v[18:33]
	s_mov_b32 m0, s35
	s_waitcnt lgkmcnt(0)
	v_mfma_f32_32x32x16_f16 v[34:49], v[132:135], v[124:127], v[34:49]
	v_mfma_f32_32x32x16_f16 v[2:17], v[132:135], v[128:131], v[2:17]
	ds_read_b128 v[120:123], v96
	ds_read_b128 v[124:127], v113
	ds_read_b128 v[128:131], v113 offset:4096
	ds_read_b128 v[132:135], v112 offset:4096
	s_waitcnt lgkmcnt(2)
	v_mfma_f32_32x32x16_f16 v[50:65], v[120:123], v[124:127], v[50:65]
	s_waitcnt lgkmcnt(1)
	v_mfma_f32_32x32x16_f16 v[18:33], v[120:123], v[128:131], v[18:33]
	s_waitcnt lgkmcnt(0)
	v_mfma_f32_32x32x16_f16 v[34:49], v[132:135], v[124:127], v[34:49]
	v_mfma_f32_32x32x16_f16 v[2:17], v[132:135], v[128:131], v[2:17]
	ds_read_b128 v[120:123], v97
	ds_read_b128 v[124:127], v115
	ds_read_b128 v[128:131], v115 offset:4096
	ds_read_b128 v[132:135], v114 offset:4096
	buffer_load_dwordx4 v72, s[4:7], s43 offen lds
	s_mov_b32 m0, s36
	s_nop 0
	buffer_load_dwordx4 v74, s[4:7], s43 offen lds
	s_mov_b32 m0, s37
	s_waitcnt lgkmcnt(2)
	v_mfma_f32_32x32x16_f16 v[50:65], v[120:123], v[124:127], v[50:65]
	buffer_load_dwordx4 v73, s[12:15], s43 offen lds
	s_mov_b32 m0, s38
	s_nop 0
	buffer_load_dwordx4 v75, s[12:15], s43 offen lds
	s_waitcnt vmcnt(8)
	s_barrier
	s_add_i32 s43, s0, 0x380
	s_waitcnt lgkmcnt(1)
	v_mfma_f32_32x32x16_f16 v[18:33], v[120:123], v[128:131], v[18:33]
	s_mov_b32 m0, s39
	s_waitcnt lgkmcnt(0)
	v_mfma_f32_32x32x16_f16 v[34:49], v[132:135], v[124:127], v[34:49]
	v_mfma_f32_32x32x16_f16 v[2:17], v[132:135], v[128:131], v[2:17]
	ds_read_b128 v[120:123], v98
	ds_read_b128 v[124:127], v117
	ds_read_b128 v[128:131], v117 offset:4096
	ds_read_b128 v[132:135], v116 offset:4096
	s_waitcnt lgkmcnt(2)
	v_mfma_f32_32x32x16_f16 v[50:65], v[120:123], v[124:127], v[50:65]
	s_waitcnt lgkmcnt(1)
	v_mfma_f32_32x32x16_f16 v[18:33], v[120:123], v[128:131], v[18:33]
	s_waitcnt lgkmcnt(0)
	v_mfma_f32_32x32x16_f16 v[34:49], v[132:135], v[124:127], v[34:49]
	v_mfma_f32_32x32x16_f16 v[2:17], v[132:135], v[128:131], v[2:17]
	ds_read_b128 v[120:123], v99
	ds_read_b128 v[124:127], v119
	ds_read_b128 v[128:131], v119 offset:4096
	ds_read_b128 v[132:135], v118 offset:4096
	buffer_load_dwordx4 v72, s[4:7], s43 offen lds
	s_mov_b32 m0, s40
	s_nop 0
	buffer_load_dwordx4 v74, s[4:7], s43 offen lds
	s_mov_b32 m0, s41
	s_waitcnt lgkmcnt(2)
	v_mfma_f32_32x32x16_f16 v[50:65], v[120:123], v[124:127], v[50:65]
	buffer_load_dwordx4 v73, s[12:15], s43 offen lds
	s_mov_b32 m0, s42
	s_nop 0
	buffer_load_dwordx4 v75, s[12:15], s43 offen lds
	s_waitcnt vmcnt(8)
	s_barrier
	s_add_i32 s43, s0, 0x400
	s_waitcnt lgkmcnt(1)
	v_mfma_f32_32x32x16_f16 v[18:33], v[120:123], v[128:131], v[18:33]
	s_mov_b32 m0, s1
	s_waitcnt lgkmcnt(0)
	v_mfma_f32_32x32x16_f16 v[34:49], v[132:135], v[124:127], v[34:49]
	v_mfma_f32_32x32x16_f16 v[2:17], v[132:135], v[128:131], v[2:17]
	ds_read_b128 v[120:123], v110 offset:16384
	ds_read_b128 v[124:127], v111
	ds_read_b128 v[128:131], v111 offset:4096
	ds_read_b128 v[132:135], v110 offset:20480
	s_waitcnt lgkmcnt(2)
	v_mfma_f32_32x32x16_f16 v[50:65], v[120:123], v[124:127], v[50:65]
	s_waitcnt lgkmcnt(1)
	v_mfma_f32_32x32x16_f16 v[18:33], v[120:123], v[128:131], v[18:33]
	s_waitcnt lgkmcnt(0)
	v_mfma_f32_32x32x16_f16 v[34:49], v[132:135], v[124:127], v[34:49]
	v_mfma_f32_32x32x16_f16 v[2:17], v[132:135], v[128:131], v[2:17]
	ds_read_b128 v[120:123], v67 offset:16384
	ds_read_b128 v[124:127], v109
	ds_read_b128 v[128:131], v109 offset:4096
	ds_read_b128 v[132:135], v67 offset:20480
	buffer_load_dwordx4 v72, s[4:7], s43 offen lds
	s_mov_b32 m0, s2
	s_nop 0
	buffer_load_dwordx4 v74, s[4:7], s43 offen lds
	s_mov_b32 m0, s3
	s_waitcnt lgkmcnt(2)
	v_mfma_f32_32x32x16_f16 v[50:65], v[120:123], v[124:127], v[50:65]
	buffer_load_dwordx4 v73, s[12:15], s43 offen lds
	s_mov_b32 m0, s18
	s_nop 0
	buffer_load_dwordx4 v75, s[12:15], s43 offen lds
	s_waitcnt vmcnt(8)
	s_barrier
	s_add_i32 s43, s0, 0x480
	s_waitcnt lgkmcnt(1)
	v_mfma_f32_32x32x16_f16 v[18:33], v[120:123], v[128:131], v[18:33]
	s_mov_b32 m0, s19
	s_waitcnt lgkmcnt(0)
	v_mfma_f32_32x32x16_f16 v[34:49], v[132:135], v[124:127], v[34:49]
	v_mfma_f32_32x32x16_f16 v[2:17], v[132:135], v[128:131], v[2:17]
	ds_read_b128 v[120:123], v110 offset:49152
	ds_read_b128 v[124:127], v111 offset:32768
	ds_read_b128 v[128:131], v111 offset:36864
	ds_read_b128 v[132:135], v110 offset:53248
	s_waitcnt lgkmcnt(2)
	v_mfma_f32_32x32x16_f16 v[50:65], v[120:123], v[124:127], v[50:65]
	s_waitcnt lgkmcnt(1)
	v_mfma_f32_32x32x16_f16 v[18:33], v[120:123], v[128:131], v[18:33]
	s_waitcnt lgkmcnt(0)
	v_mfma_f32_32x32x16_f16 v[34:49], v[132:135], v[124:127], v[34:49]
	v_mfma_f32_32x32x16_f16 v[2:17], v[132:135], v[128:131], v[2:17]
	ds_read_b128 v[120:123], v67 offset:49152
	ds_read_b128 v[124:127], v109 offset:32768
	ds_read_b128 v[128:131], v109 offset:36864
	ds_read_b128 v[132:135], v67 offset:53248
	buffer_load_dwordx4 v72, s[4:7], s43 offen lds
	s_mov_b32 m0, s31
	s_nop 0
	buffer_load_dwordx4 v74, s[4:7], s43 offen lds
	s_mov_b32 m0, s33
	s_waitcnt lgkmcnt(2)
	v_mfma_f32_32x32x16_f16 v[50:65], v[120:123], v[124:127], v[50:65]
	buffer_load_dwordx4 v73, s[12:15], s43 offen lds
	s_mov_b32 m0, s34
	s_nop 0
	buffer_load_dwordx4 v75, s[12:15], s43 offen lds
	s_waitcnt vmcnt(8)
	s_barrier
	s_add_i32 s43, s0, 0x500
	s_waitcnt lgkmcnt(1)
	v_mfma_f32_32x32x16_f16 v[18:33], v[120:123], v[128:131], v[18:33]
	s_mov_b32 m0, s35
	s_waitcnt lgkmcnt(0)
	v_mfma_f32_32x32x16_f16 v[34:49], v[132:135], v[124:127], v[34:49]
	v_mfma_f32_32x32x16_f16 v[2:17], v[132:135], v[128:131], v[2:17]
	ds_read_b128 v[120:123], v96
	ds_read_b128 v[124:127], v113
	ds_read_b128 v[128:131], v113 offset:4096
	ds_read_b128 v[132:135], v112 offset:4096
	s_waitcnt lgkmcnt(2)
	v_mfma_f32_32x32x16_f16 v[50:65], v[120:123], v[124:127], v[50:65]
	s_waitcnt lgkmcnt(1)
	v_mfma_f32_32x32x16_f16 v[18:33], v[120:123], v[128:131], v[18:33]
	s_waitcnt lgkmcnt(0)
	v_mfma_f32_32x32x16_f16 v[34:49], v[132:135], v[124:127], v[34:49]
	v_mfma_f32_32x32x16_f16 v[2:17], v[132:135], v[128:131], v[2:17]
	ds_read_b128 v[120:123], v97
	ds_read_b128 v[124:127], v115
	ds_read_b128 v[128:131], v115 offset:4096
	ds_read_b128 v[132:135], v114 offset:4096
	buffer_load_dwordx4 v72, s[4:7], s43 offen lds
	s_mov_b32 m0, s36
	s_nop 0
	buffer_load_dwordx4 v74, s[4:7], s43 offen lds
	s_mov_b32 m0, s37
	s_waitcnt lgkmcnt(2)
	v_mfma_f32_32x32x16_f16 v[50:65], v[120:123], v[124:127], v[50:65]
	buffer_load_dwordx4 v73, s[12:15], s43 offen lds
	s_mov_b32 m0, s38
	s_nop 0
	buffer_load_dwordx4 v75, s[12:15], s43 offen lds
	s_waitcnt vmcnt(8)
	s_barrier
	s_add_i32 s43, s0, 0x580
	s_waitcnt lgkmcnt(1)
	v_mfma_f32_32x32x16_f16 v[18:33], v[120:123], v[128:131], v[18:33]
	s_mov_b32 m0, s39
	s_waitcnt lgkmcnt(0)
	v_mfma_f32_32x32x16_f16 v[34:49], v[132:135], v[124:127], v[34:49]
	v_mfma_f32_32x32x16_f16 v[2:17], v[132:135], v[128:131], v[2:17]
	ds_read_b128 v[120:123], v98
	ds_read_b128 v[124:127], v117
	ds_read_b128 v[128:131], v117 offset:4096
	ds_read_b128 v[132:135], v116 offset:4096
	s_waitcnt lgkmcnt(2)
	v_mfma_f32_32x32x16_f16 v[50:65], v[120:123], v[124:127], v[50:65]
	s_waitcnt lgkmcnt(1)
	v_mfma_f32_32x32x16_f16 v[18:33], v[120:123], v[128:131], v[18:33]
	s_waitcnt lgkmcnt(0)
	v_mfma_f32_32x32x16_f16 v[34:49], v[132:135], v[124:127], v[34:49]
	v_mfma_f32_32x32x16_f16 v[2:17], v[132:135], v[128:131], v[2:17]
	ds_read_b128 v[120:123], v99
	ds_read_b128 v[124:127], v119
	ds_read_b128 v[128:131], v119 offset:4096
	ds_read_b128 v[132:135], v118 offset:4096
	buffer_load_dwordx4 v72, s[4:7], s43 offen lds
	s_mov_b32 m0, s40
	s_nop 0
	buffer_load_dwordx4 v74, s[4:7], s43 offen lds
	s_mov_b32 m0, s41
	s_waitcnt lgkmcnt(2)
	v_mfma_f32_32x32x16_f16 v[50:65], v[120:123], v[124:127], v[50:65]
	buffer_load_dwordx4 v73, s[12:15], s43 offen lds
	s_mov_b32 m0, s42
	s_nop 0
	buffer_load_dwordx4 v75, s[12:15], s43 offen lds
	s_waitcnt vmcnt(8)
	s_barrier
	s_add_i32 s43, s0, 0x600
	s_waitcnt lgkmcnt(1)
	v_mfma_f32_32x32x16_f16 v[18:33], v[120:123], v[128:131], v[18:33]
	s_mov_b32 m0, s1
	s_waitcnt lgkmcnt(0)
	v_mfma_f32_32x32x16_f16 v[34:49], v[132:135], v[124:127], v[34:49]
	v_mfma_f32_32x32x16_f16 v[2:17], v[132:135], v[128:131], v[2:17]
	ds_read_b128 v[120:123], v110 offset:16384
	ds_read_b128 v[124:127], v111
	ds_read_b128 v[128:131], v111 offset:4096
	ds_read_b128 v[132:135], v110 offset:20480
	s_waitcnt lgkmcnt(2)
	v_mfma_f32_32x32x16_f16 v[50:65], v[120:123], v[124:127], v[50:65]
	s_waitcnt lgkmcnt(1)
	v_mfma_f32_32x32x16_f16 v[18:33], v[120:123], v[128:131], v[18:33]
	s_waitcnt lgkmcnt(0)
	v_mfma_f32_32x32x16_f16 v[34:49], v[132:135], v[124:127], v[34:49]
	v_mfma_f32_32x32x16_f16 v[2:17], v[132:135], v[128:131], v[2:17]
	ds_read_b128 v[120:123], v67 offset:16384
	ds_read_b128 v[124:127], v109
	ds_read_b128 v[128:131], v109 offset:4096
	ds_read_b128 v[132:135], v67 offset:20480
	buffer_load_dwordx4 v72, s[4:7], s43 offen lds
	s_mov_b32 m0, s2
	s_nop 0
	buffer_load_dwordx4 v74, s[4:7], s43 offen lds
	s_mov_b32 m0, s3
	s_waitcnt lgkmcnt(2)
	v_mfma_f32_32x32x16_f16 v[50:65], v[120:123], v[124:127], v[50:65]
	buffer_load_dwordx4 v73, s[12:15], s43 offen lds
	s_mov_b32 m0, s18
	s_nop 0
	buffer_load_dwordx4 v75, s[12:15], s43 offen lds
	s_waitcnt vmcnt(8)
	s_barrier
	s_add_i32 s43, s0, 0x680
	s_waitcnt lgkmcnt(1)
	v_mfma_f32_32x32x16_f16 v[18:33], v[120:123], v[128:131], v[18:33]
	s_mov_b32 m0, s19
	s_waitcnt lgkmcnt(0)
	v_mfma_f32_32x32x16_f16 v[34:49], v[132:135], v[124:127], v[34:49]
	v_mfma_f32_32x32x16_f16 v[2:17], v[132:135], v[128:131], v[2:17]
	ds_read_b128 v[120:123], v110 offset:49152
	ds_read_b128 v[124:127], v111 offset:32768
	ds_read_b128 v[128:131], v111 offset:36864
	ds_read_b128 v[132:135], v110 offset:53248
	s_waitcnt lgkmcnt(2)
	v_mfma_f32_32x32x16_f16 v[50:65], v[120:123], v[124:127], v[50:65]
	s_waitcnt lgkmcnt(1)
	v_mfma_f32_32x32x16_f16 v[18:33], v[120:123], v[128:131], v[18:33]
	s_waitcnt lgkmcnt(0)
	v_mfma_f32_32x32x16_f16 v[34:49], v[132:135], v[124:127], v[34:49]
	v_mfma_f32_32x32x16_f16 v[2:17], v[132:135], v[128:131], v[2:17]
	ds_read_b128 v[120:123], v67 offset:49152
	ds_read_b128 v[124:127], v109 offset:32768
	ds_read_b128 v[128:131], v109 offset:36864
	ds_read_b128 v[132:135], v67 offset:53248
	buffer_load_dwordx4 v72, s[4:7], s43 offen lds
	s_mov_b32 m0, s31
	s_nop 0
	buffer_load_dwordx4 v74, s[4:7], s43 offen lds
	s_mov_b32 m0, s33
	s_waitcnt lgkmcnt(2)
	v_mfma_f32_32x32x16_f16 v[50:65], v[120:123], v[124:127], v[50:65]
	buffer_load_dwordx4 v73, s[12:15], s43 offen lds
	s_mov_b32 m0, s34
	s_nop 0
	buffer_load_dwordx4 v75, s[12:15], s43 offen lds
	s_waitcnt vmcnt(8)
	s_barrier
	s_add_i32 s43, s0, 0x700
	s_waitcnt lgkmcnt(1)
	v_mfma_f32_32x32x16_f16 v[18:33], v[120:123], v[128:131], v[18:33]
	s_mov_b32 m0, s35
	s_waitcnt lgkmcnt(0)
	v_mfma_f32_32x32x16_f16 v[34:49], v[132:135], v[124:127], v[34:49]
	v_mfma_f32_32x32x16_f16 v[2:17], v[132:135], v[128:131], v[2:17]
	ds_read_b128 v[120:123], v96
	ds_read_b128 v[124:127], v113
	ds_read_b128 v[128:131], v113 offset:4096
	ds_read_b128 v[132:135], v112 offset:4096
	s_waitcnt lgkmcnt(2)
	v_mfma_f32_32x32x16_f16 v[50:65], v[120:123], v[124:127], v[50:65]
	s_waitcnt lgkmcnt(1)
	v_mfma_f32_32x32x16_f16 v[18:33], v[120:123], v[128:131], v[18:33]
	s_waitcnt lgkmcnt(0)
	v_mfma_f32_32x32x16_f16 v[34:49], v[132:135], v[124:127], v[34:49]
	v_mfma_f32_32x32x16_f16 v[2:17], v[132:135], v[128:131], v[2:17]
	ds_read_b128 v[120:123], v97
	ds_read_b128 v[124:127], v115
	ds_read_b128 v[128:131], v115 offset:4096
	ds_read_b128 v[132:135], v114 offset:4096
	buffer_load_dwordx4 v72, s[4:7], s43 offen lds
	s_mov_b32 m0, s36
	s_nop 0
	buffer_load_dwordx4 v74, s[4:7], s43 offen lds
	s_mov_b32 m0, s37
	s_waitcnt lgkmcnt(2)
	v_mfma_f32_32x32x16_f16 v[50:65], v[120:123], v[124:127], v[50:65]
	buffer_load_dwordx4 v73, s[12:15], s43 offen lds
	s_mov_b32 m0, s38
	s_nop 0
	buffer_load_dwordx4 v75, s[12:15], s43 offen lds
	s_waitcnt vmcnt(8)
	s_barrier
	s_add_i32 s43, s0, 0x780
	s_waitcnt lgkmcnt(1)
	v_mfma_f32_32x32x16_f16 v[18:33], v[120:123], v[128:131], v[18:33]
	s_mov_b32 m0, s39
	s_waitcnt lgkmcnt(0)
	v_mfma_f32_32x32x16_f16 v[34:49], v[132:135], v[124:127], v[34:49]
	v_mfma_f32_32x32x16_f16 v[2:17], v[132:135], v[128:131], v[2:17]
	ds_read_b128 v[120:123], v98
	ds_read_b128 v[124:127], v117
	ds_read_b128 v[128:131], v117 offset:4096
	ds_read_b128 v[132:135], v116 offset:4096
	s_waitcnt lgkmcnt(2)
	v_mfma_f32_32x32x16_f16 v[50:65], v[120:123], v[124:127], v[50:65]
	s_waitcnt lgkmcnt(1)
	v_mfma_f32_32x32x16_f16 v[18:33], v[120:123], v[128:131], v[18:33]
	s_waitcnt lgkmcnt(0)
	v_mfma_f32_32x32x16_f16 v[34:49], v[132:135], v[124:127], v[34:49]
	v_mfma_f32_32x32x16_f16 v[2:17], v[132:135], v[128:131], v[2:17]
	ds_read_b128 v[120:123], v99
	ds_read_b128 v[124:127], v119
	ds_read_b128 v[128:131], v119 offset:4096
	ds_read_b128 v[132:135], v118 offset:4096
	buffer_load_dwordx4 v72, s[4:7], s43 offen lds
	s_mov_b32 m0, s40
	s_nop 0
	buffer_load_dwordx4 v74, s[4:7], s43 offen lds
	s_mov_b32 m0, s41
	s_waitcnt lgkmcnt(2)
	v_mfma_f32_32x32x16_f16 v[50:65], v[120:123], v[124:127], v[50:65]
	buffer_load_dwordx4 v73, s[12:15], s43 offen lds
	s_mov_b32 m0, s42
	s_nop 0
	buffer_load_dwordx4 v75, s[12:15], s43 offen lds
	s_waitcnt vmcnt(8)
	s_barrier
	s_add_i32 s43, s0, 0x800
	s_waitcnt lgkmcnt(1)
	v_mfma_f32_32x32x16_f16 v[18:33], v[120:123], v[128:131], v[18:33]
	s_mov_b32 m0, s1
	s_waitcnt lgkmcnt(0)
	v_mfma_f32_32x32x16_f16 v[34:49], v[132:135], v[124:127], v[34:49]
	v_mfma_f32_32x32x16_f16 v[2:17], v[132:135], v[128:131], v[2:17]
	ds_read_b128 v[120:123], v110 offset:16384
	ds_read_b128 v[124:127], v111
	ds_read_b128 v[128:131], v111 offset:4096
	ds_read_b128 v[132:135], v110 offset:20480
	s_waitcnt lgkmcnt(2)
	v_mfma_f32_32x32x16_f16 v[50:65], v[120:123], v[124:127], v[50:65]
	s_waitcnt lgkmcnt(1)
	v_mfma_f32_32x32x16_f16 v[18:33], v[120:123], v[128:131], v[18:33]
	s_waitcnt lgkmcnt(0)
	v_mfma_f32_32x32x16_f16 v[34:49], v[132:135], v[124:127], v[34:49]
	v_mfma_f32_32x32x16_f16 v[2:17], v[132:135], v[128:131], v[2:17]
	ds_read_b128 v[120:123], v67 offset:16384
	ds_read_b128 v[124:127], v109
	ds_read_b128 v[128:131], v109 offset:4096
	ds_read_b128 v[132:135], v67 offset:20480
	buffer_load_dwordx4 v72, s[4:7], s43 offen lds
	s_mov_b32 m0, s2
	s_nop 0
	buffer_load_dwordx4 v74, s[4:7], s43 offen lds
	s_mov_b32 m0, s3
	s_waitcnt lgkmcnt(2)
	v_mfma_f32_32x32x16_f16 v[50:65], v[120:123], v[124:127], v[50:65]
	buffer_load_dwordx4 v73, s[12:15], s43 offen lds
	s_mov_b32 m0, s18
	s_nop 0
	buffer_load_dwordx4 v75, s[12:15], s43 offen lds
	s_waitcnt vmcnt(8)
	s_barrier
	s_add_i32 s43, s0, 0x880
	s_waitcnt lgkmcnt(1)
	v_mfma_f32_32x32x16_f16 v[18:33], v[120:123], v[128:131], v[18:33]
	s_mov_b32 m0, s19
	s_waitcnt lgkmcnt(0)
	v_mfma_f32_32x32x16_f16 v[34:49], v[132:135], v[124:127], v[34:49]
	v_mfma_f32_32x32x16_f16 v[2:17], v[132:135], v[128:131], v[2:17]
	ds_read_b128 v[120:123], v110 offset:49152
	ds_read_b128 v[124:127], v111 offset:32768
	ds_read_b128 v[128:131], v111 offset:36864
	ds_read_b128 v[132:135], v110 offset:53248
	s_waitcnt lgkmcnt(2)
	v_mfma_f32_32x32x16_f16 v[50:65], v[120:123], v[124:127], v[50:65]
	s_waitcnt lgkmcnt(1)
	v_mfma_f32_32x32x16_f16 v[18:33], v[120:123], v[128:131], v[18:33]
	s_waitcnt lgkmcnt(0)
	v_mfma_f32_32x32x16_f16 v[34:49], v[132:135], v[124:127], v[34:49]
	v_mfma_f32_32x32x16_f16 v[2:17], v[132:135], v[128:131], v[2:17]
	ds_read_b128 v[120:123], v67 offset:49152
	ds_read_b128 v[124:127], v109 offset:32768
	ds_read_b128 v[128:131], v109 offset:36864
	ds_read_b128 v[132:135], v67 offset:53248
	buffer_load_dwordx4 v72, s[4:7], s43 offen lds
	s_mov_b32 m0, s31
	s_nop 0
	buffer_load_dwordx4 v74, s[4:7], s43 offen lds
	s_mov_b32 m0, s33
	s_waitcnt lgkmcnt(2)
	v_mfma_f32_32x32x16_f16 v[50:65], v[120:123], v[124:127], v[50:65]
	buffer_load_dwordx4 v73, s[12:15], s43 offen lds
	s_mov_b32 m0, s34
	s_nop 0
	buffer_load_dwordx4 v75, s[12:15], s43 offen lds
	s_waitcnt vmcnt(8)
	s_barrier
	s_add_i32 s43, s0, 0x900
	s_waitcnt lgkmcnt(1)
	v_mfma_f32_32x32x16_f16 v[18:33], v[120:123], v[128:131], v[18:33]
	s_mov_b32 m0, s35
	s_waitcnt lgkmcnt(0)
	v_mfma_f32_32x32x16_f16 v[34:49], v[132:135], v[124:127], v[34:49]
	v_mfma_f32_32x32x16_f16 v[2:17], v[132:135], v[128:131], v[2:17]
	ds_read_b128 v[120:123], v96
	ds_read_b128 v[124:127], v113
	ds_read_b128 v[128:131], v113 offset:4096
	ds_read_b128 v[132:135], v112 offset:4096
	s_waitcnt lgkmcnt(2)
	v_mfma_f32_32x32x16_f16 v[50:65], v[120:123], v[124:127], v[50:65]
	s_waitcnt lgkmcnt(1)
	v_mfma_f32_32x32x16_f16 v[18:33], v[120:123], v[128:131], v[18:33]
	s_waitcnt lgkmcnt(0)
	v_mfma_f32_32x32x16_f16 v[34:49], v[132:135], v[124:127], v[34:49]
	v_mfma_f32_32x32x16_f16 v[2:17], v[132:135], v[128:131], v[2:17]
	ds_read_b128 v[120:123], v97
	ds_read_b128 v[124:127], v115
	ds_read_b128 v[128:131], v115 offset:4096
	ds_read_b128 v[132:135], v114 offset:4096
	buffer_load_dwordx4 v72, s[4:7], s43 offen lds
	s_mov_b32 m0, s36
	s_nop 0
	buffer_load_dwordx4 v74, s[4:7], s43 offen lds
	s_mov_b32 m0, s37
	s_waitcnt lgkmcnt(2)
	v_mfma_f32_32x32x16_f16 v[50:65], v[120:123], v[124:127], v[50:65]
	buffer_load_dwordx4 v73, s[12:15], s43 offen lds
	s_mov_b32 m0, s38
	s_nop 0
	buffer_load_dwordx4 v75, s[12:15], s43 offen lds
	s_waitcnt vmcnt(8)
	s_barrier
	s_add_i32 s43, s0, 0x980
	s_waitcnt lgkmcnt(1)
	v_mfma_f32_32x32x16_f16 v[18:33], v[120:123], v[128:131], v[18:33]
	s_mov_b32 m0, s39
	s_waitcnt lgkmcnt(0)
	v_mfma_f32_32x32x16_f16 v[34:49], v[132:135], v[124:127], v[34:49]
	v_mfma_f32_32x32x16_f16 v[2:17], v[132:135], v[128:131], v[2:17]
	ds_read_b128 v[120:123], v98
	ds_read_b128 v[124:127], v117
	ds_read_b128 v[128:131], v117 offset:4096
	ds_read_b128 v[132:135], v116 offset:4096
	s_waitcnt lgkmcnt(2)
	v_mfma_f32_32x32x16_f16 v[50:65], v[120:123], v[124:127], v[50:65]
	s_waitcnt lgkmcnt(1)
	v_mfma_f32_32x32x16_f16 v[18:33], v[120:123], v[128:131], v[18:33]
	s_waitcnt lgkmcnt(0)
	v_mfma_f32_32x32x16_f16 v[34:49], v[132:135], v[124:127], v[34:49]
	v_mfma_f32_32x32x16_f16 v[2:17], v[132:135], v[128:131], v[2:17]
	ds_read_b128 v[120:123], v99
	ds_read_b128 v[124:127], v119
	ds_read_b128 v[128:131], v119 offset:4096
	ds_read_b128 v[132:135], v118 offset:4096
	buffer_load_dwordx4 v72, s[4:7], s43 offen lds
	s_mov_b32 m0, s40
	s_nop 0
	buffer_load_dwordx4 v74, s[4:7], s43 offen lds
	s_mov_b32 m0, s41
	s_waitcnt lgkmcnt(2)
	v_mfma_f32_32x32x16_f16 v[50:65], v[120:123], v[124:127], v[50:65]
	buffer_load_dwordx4 v73, s[12:15], s43 offen lds
	s_mov_b32 m0, s42
	s_nop 0
	buffer_load_dwordx4 v75, s[12:15], s43 offen lds
	s_waitcnt vmcnt(8)
	s_barrier
	s_add_i32 s43, s0, 0xa00
	s_waitcnt lgkmcnt(1)
	v_mfma_f32_32x32x16_f16 v[18:33], v[120:123], v[128:131], v[18:33]
	s_mov_b32 m0, s1
	s_waitcnt lgkmcnt(0)
	v_mfma_f32_32x32x16_f16 v[34:49], v[132:135], v[124:127], v[34:49]
	v_mfma_f32_32x32x16_f16 v[2:17], v[132:135], v[128:131], v[2:17]
	ds_read_b128 v[120:123], v110 offset:16384
	ds_read_b128 v[124:127], v111
	ds_read_b128 v[128:131], v111 offset:4096
	ds_read_b128 v[132:135], v110 offset:20480
	s_waitcnt lgkmcnt(2)
	v_mfma_f32_32x32x16_f16 v[50:65], v[120:123], v[124:127], v[50:65]
	s_waitcnt lgkmcnt(1)
	v_mfma_f32_32x32x16_f16 v[18:33], v[120:123], v[128:131], v[18:33]
	s_waitcnt lgkmcnt(0)
	v_mfma_f32_32x32x16_f16 v[34:49], v[132:135], v[124:127], v[34:49]
	v_mfma_f32_32x32x16_f16 v[2:17], v[132:135], v[128:131], v[2:17]
	ds_read_b128 v[120:123], v67 offset:16384
	ds_read_b128 v[124:127], v109
	ds_read_b128 v[128:131], v109 offset:4096
	ds_read_b128 v[132:135], v67 offset:20480
	buffer_load_dwordx4 v72, s[4:7], s43 offen lds
	s_mov_b32 m0, s2
	s_nop 0
	buffer_load_dwordx4 v74, s[4:7], s43 offen lds
	s_mov_b32 m0, s3
	s_waitcnt lgkmcnt(2)
	v_mfma_f32_32x32x16_f16 v[50:65], v[120:123], v[124:127], v[50:65]
	buffer_load_dwordx4 v73, s[12:15], s43 offen lds
	s_mov_b32 m0, s18
	s_nop 0
	buffer_load_dwordx4 v75, s[12:15], s43 offen lds
	s_waitcnt vmcnt(8)
	s_barrier
	s_add_i32 s43, s0, 0xa80
	s_waitcnt lgkmcnt(1)
	v_mfma_f32_32x32x16_f16 v[18:33], v[120:123], v[128:131], v[18:33]
	s_mov_b32 m0, s19
	s_waitcnt lgkmcnt(0)
	v_mfma_f32_32x32x16_f16 v[34:49], v[132:135], v[124:127], v[34:49]
	v_mfma_f32_32x32x16_f16 v[2:17], v[132:135], v[128:131], v[2:17]
	ds_read_b128 v[120:123], v110 offset:49152
	ds_read_b128 v[124:127], v111 offset:32768
	ds_read_b128 v[128:131], v111 offset:36864
	ds_read_b128 v[132:135], v110 offset:53248
	s_waitcnt lgkmcnt(2)
	v_mfma_f32_32x32x16_f16 v[50:65], v[120:123], v[124:127], v[50:65]
	s_waitcnt lgkmcnt(1)
	v_mfma_f32_32x32x16_f16 v[18:33], v[120:123], v[128:131], v[18:33]
	s_waitcnt lgkmcnt(0)
	v_mfma_f32_32x32x16_f16 v[34:49], v[132:135], v[124:127], v[34:49]
	v_mfma_f32_32x32x16_f16 v[2:17], v[132:135], v[128:131], v[2:17]
	ds_read_b128 v[120:123], v67 offset:49152
	ds_read_b128 v[124:127], v109 offset:32768
	ds_read_b128 v[128:131], v109 offset:36864
	ds_read_b128 v[132:135], v67 offset:53248
	buffer_load_dwordx4 v72, s[4:7], s43 offen lds
	s_mov_b32 m0, s31
	s_nop 0
	buffer_load_dwordx4 v74, s[4:7], s43 offen lds
	s_mov_b32 m0, s33
	s_waitcnt lgkmcnt(2)
	v_mfma_f32_32x32x16_f16 v[50:65], v[120:123], v[124:127], v[50:65]
	buffer_load_dwordx4 v73, s[12:15], s43 offen lds
	s_mov_b32 m0, s34
	s_nop 0
	buffer_load_dwordx4 v75, s[12:15], s43 offen lds
	s_waitcnt vmcnt(8)
	s_barrier
	s_add_i32 s43, s0, 0xb00
	s_waitcnt lgkmcnt(1)
	v_mfma_f32_32x32x16_f16 v[18:33], v[120:123], v[128:131], v[18:33]
	s_mov_b32 m0, s35
	s_waitcnt lgkmcnt(0)
	v_mfma_f32_32x32x16_f16 v[34:49], v[132:135], v[124:127], v[34:49]
	v_mfma_f32_32x32x16_f16 v[2:17], v[132:135], v[128:131], v[2:17]
	ds_read_b128 v[120:123], v96
	ds_read_b128 v[124:127], v113
	ds_read_b128 v[128:131], v113 offset:4096
	ds_read_b128 v[132:135], v112 offset:4096
	s_waitcnt lgkmcnt(2)
	v_mfma_f32_32x32x16_f16 v[50:65], v[120:123], v[124:127], v[50:65]
	s_waitcnt lgkmcnt(1)
	v_mfma_f32_32x32x16_f16 v[18:33], v[120:123], v[128:131], v[18:33]
	s_waitcnt lgkmcnt(0)
	v_mfma_f32_32x32x16_f16 v[34:49], v[132:135], v[124:127], v[34:49]
	v_mfma_f32_32x32x16_f16 v[2:17], v[132:135], v[128:131], v[2:17]
	ds_read_b128 v[120:123], v97
	ds_read_b128 v[124:127], v115
	ds_read_b128 v[128:131], v115 offset:4096
	ds_read_b128 v[132:135], v114 offset:4096
	buffer_load_dwordx4 v72, s[4:7], s43 offen lds
	s_mov_b32 m0, s36
	s_nop 0
	buffer_load_dwordx4 v74, s[4:7], s43 offen lds
	s_mov_b32 m0, s37
	s_waitcnt lgkmcnt(2)
	v_mfma_f32_32x32x16_f16 v[50:65], v[120:123], v[124:127], v[50:65]
	buffer_load_dwordx4 v73, s[12:15], s43 offen lds
	s_mov_b32 m0, s38
	s_nop 0
	buffer_load_dwordx4 v75, s[12:15], s43 offen lds
	s_waitcnt vmcnt(8)
	s_barrier
	s_add_i32 s43, s0, 0xb80
	s_waitcnt lgkmcnt(1)
	v_mfma_f32_32x32x16_f16 v[18:33], v[120:123], v[128:131], v[18:33]
	s_mov_b32 m0, s39
	s_waitcnt lgkmcnt(0)
	v_mfma_f32_32x32x16_f16 v[34:49], v[132:135], v[124:127], v[34:49]
	v_mfma_f32_32x32x16_f16 v[2:17], v[132:135], v[128:131], v[2:17]
	ds_read_b128 v[120:123], v98
	ds_read_b128 v[124:127], v117
	ds_read_b128 v[128:131], v117 offset:4096
	ds_read_b128 v[132:135], v116 offset:4096
	s_waitcnt lgkmcnt(2)
	v_mfma_f32_32x32x16_f16 v[50:65], v[120:123], v[124:127], v[50:65]
	s_waitcnt lgkmcnt(1)
	v_mfma_f32_32x32x16_f16 v[18:33], v[120:123], v[128:131], v[18:33]
	s_waitcnt lgkmcnt(0)
	v_mfma_f32_32x32x16_f16 v[34:49], v[132:135], v[124:127], v[34:49]
	v_mfma_f32_32x32x16_f16 v[2:17], v[132:135], v[128:131], v[2:17]
	ds_read_b128 v[120:123], v99
	ds_read_b128 v[124:127], v119
	ds_read_b128 v[128:131], v119 offset:4096
	ds_read_b128 v[132:135], v118 offset:4096
	buffer_load_dwordx4 v72, s[4:7], s43 offen lds
	s_mov_b32 m0, s40
	s_nop 0
	buffer_load_dwordx4 v74, s[4:7], s43 offen lds
	s_mov_b32 m0, s41
	s_waitcnt lgkmcnt(2)
	v_mfma_f32_32x32x16_f16 v[50:65], v[120:123], v[124:127], v[50:65]
	buffer_load_dwordx4 v73, s[12:15], s43 offen lds
	s_mov_b32 m0, s42
	s_nop 0
	buffer_load_dwordx4 v75, s[12:15], s43 offen lds
	s_waitcnt vmcnt(8)
	s_barrier
	s_add_i32 s43, s0, 0xc00
	s_waitcnt lgkmcnt(1)
	v_mfma_f32_32x32x16_f16 v[18:33], v[120:123], v[128:131], v[18:33]
	s_mov_b32 m0, s1
	s_waitcnt lgkmcnt(0)
	v_mfma_f32_32x32x16_f16 v[34:49], v[132:135], v[124:127], v[34:49]
	v_mfma_f32_32x32x16_f16 v[2:17], v[132:135], v[128:131], v[2:17]
	ds_read_b128 v[120:123], v110 offset:16384
	ds_read_b128 v[124:127], v111
	ds_read_b128 v[128:131], v111 offset:4096
	ds_read_b128 v[132:135], v110 offset:20480
	s_waitcnt lgkmcnt(2)
	v_mfma_f32_32x32x16_f16 v[50:65], v[120:123], v[124:127], v[50:65]
	s_waitcnt lgkmcnt(1)
	v_mfma_f32_32x32x16_f16 v[18:33], v[120:123], v[128:131], v[18:33]
	s_waitcnt lgkmcnt(0)
	v_mfma_f32_32x32x16_f16 v[34:49], v[132:135], v[124:127], v[34:49]
	v_mfma_f32_32x32x16_f16 v[2:17], v[132:135], v[128:131], v[2:17]
	ds_read_b128 v[120:123], v67 offset:16384
	ds_read_b128 v[124:127], v109
	ds_read_b128 v[128:131], v109 offset:4096
	ds_read_b128 v[132:135], v67 offset:20480
	buffer_load_dwordx4 v72, s[4:7], s43 offen lds
	s_mov_b32 m0, s2
	s_nop 0
	buffer_load_dwordx4 v74, s[4:7], s43 offen lds
	s_mov_b32 m0, s3
	s_waitcnt lgkmcnt(2)
	v_mfma_f32_32x32x16_f16 v[50:65], v[120:123], v[124:127], v[50:65]
	buffer_load_dwordx4 v73, s[12:15], s43 offen lds
	s_mov_b32 m0, s18
	s_nop 0
	buffer_load_dwordx4 v75, s[12:15], s43 offen lds
	s_waitcnt vmcnt(8)
	s_barrier
	s_add_i32 s43, s0, 0xc80
	s_waitcnt lgkmcnt(1)
	v_mfma_f32_32x32x16_f16 v[18:33], v[120:123], v[128:131], v[18:33]
	s_mov_b32 m0, s19
	s_add_i32 s19, s0, 0xd00
	s_waitcnt lgkmcnt(0)
	v_mfma_f32_32x32x16_f16 v[34:49], v[132:135], v[124:127], v[34:49]
	v_mfma_f32_32x32x16_f16 v[2:17], v[132:135], v[128:131], v[2:17]
	ds_read_b128 v[120:123], v110 offset:49152
	ds_read_b128 v[124:127], v111 offset:32768
	ds_read_b128 v[128:131], v111 offset:36864
	ds_read_b128 v[132:135], v110 offset:53248
	s_waitcnt lgkmcnt(2)
	v_mfma_f32_32x32x16_f16 v[50:65], v[120:123], v[124:127], v[50:65]
	s_waitcnt lgkmcnt(1)
	v_mfma_f32_32x32x16_f16 v[18:33], v[120:123], v[128:131], v[18:33]
	s_waitcnt lgkmcnt(0)
	v_mfma_f32_32x32x16_f16 v[34:49], v[132:135], v[124:127], v[34:49]
	v_mfma_f32_32x32x16_f16 v[2:17], v[132:135], v[128:131], v[2:17]
	ds_read_b128 v[120:123], v67 offset:49152
	ds_read_b128 v[124:127], v109 offset:32768
	ds_read_b128 v[128:131], v109 offset:36864
	ds_read_b128 v[132:135], v67 offset:53248
	buffer_load_dwordx4 v72, s[4:7], s43 offen lds
	s_mov_b32 m0, s31
	s_add_i32 s31, s0, 0xe00
	buffer_load_dwordx4 v74, s[4:7], s43 offen lds
	s_mov_b32 m0, s33
	s_waitcnt lgkmcnt(2)
	v_mfma_f32_32x32x16_f16 v[50:65], v[120:123], v[124:127], v[50:65]
	buffer_load_dwordx4 v73, s[12:15], s43 offen lds
	s_mov_b32 m0, s34
	s_nop 0
	buffer_load_dwordx4 v75, s[12:15], s43 offen lds
	s_waitcnt vmcnt(8)
	s_barrier
	s_mov_b32 m0, s35
	s_waitcnt lgkmcnt(1)
	v_mfma_f32_32x32x16_f16 v[18:33], v[120:123], v[128:131], v[18:33]
	s_waitcnt lgkmcnt(0)
	v_mfma_f32_32x32x16_f16 v[34:49], v[132:135], v[124:127], v[34:49]
	v_mfma_f32_32x32x16_f16 v[2:17], v[132:135], v[128:131], v[2:17]
	ds_read_b128 v[120:123], v96
	ds_read_b128 v[124:127], v113
	ds_read_b128 v[128:131], v113 offset:4096
	ds_read_b128 v[132:135], v112 offset:4096
	s_waitcnt lgkmcnt(2)
	v_mfma_f32_32x32x16_f16 v[50:65], v[120:123], v[124:127], v[50:65]
	s_waitcnt lgkmcnt(1)
	v_mfma_f32_32x32x16_f16 v[18:33], v[120:123], v[128:131], v[18:33]
	s_waitcnt lgkmcnt(0)
	v_mfma_f32_32x32x16_f16 v[34:49], v[132:135], v[124:127], v[34:49]
	v_mfma_f32_32x32x16_f16 v[2:17], v[132:135], v[128:131], v[2:17]
	ds_read_b128 v[120:123], v97
	ds_read_b128 v[124:127], v115
	ds_read_b128 v[128:131], v115 offset:4096
	ds_read_b128 v[132:135], v114 offset:4096
	buffer_load_dwordx4 v72, s[4:7], s19 offen lds
	s_mov_b32 m0, s36
	s_nop 0
	buffer_load_dwordx4 v74, s[4:7], s19 offen lds
	s_mov_b32 m0, s37
	s_waitcnt lgkmcnt(2)
	v_mfma_f32_32x32x16_f16 v[50:65], v[120:123], v[124:127], v[50:65]
	buffer_load_dwordx4 v73, s[12:15], s19 offen lds
	s_mov_b32 m0, s38
	s_nop 0
	buffer_load_dwordx4 v75, s[12:15], s19 offen lds
	s_waitcnt vmcnt(8)
	s_barrier
	s_add_i32 s19, s0, 0xd80
	s_waitcnt lgkmcnt(1)
	v_mfma_f32_32x32x16_f16 v[18:33], v[120:123], v[128:131], v[18:33]
	s_mov_b32 m0, s39
	s_ashr_i32 s0, s23, 31
	s_xor_b32 s0, s0, s25
	s_waitcnt lgkmcnt(0)
	v_mfma_f32_32x32x16_f16 v[34:49], v[132:135], v[124:127], v[34:49]
	v_mfma_f32_32x32x16_f16 v[2:17], v[132:135], v[128:131], v[2:17]
	ds_read_b128 v[120:123], v98
	ds_read_b128 v[124:127], v117
	ds_read_b128 v[128:131], v117 offset:4096
	ds_read_b128 v[132:135], v116 offset:4096
	s_waitcnt lgkmcnt(2)
	v_mfma_f32_32x32x16_f16 v[50:65], v[120:123], v[124:127], v[50:65]
	s_waitcnt lgkmcnt(1)
	v_mfma_f32_32x32x16_f16 v[18:33], v[120:123], v[128:131], v[18:33]
	s_waitcnt lgkmcnt(0)
	v_mfma_f32_32x32x16_f16 v[34:49], v[132:135], v[124:127], v[34:49]
	v_mfma_f32_32x32x16_f16 v[2:17], v[132:135], v[128:131], v[2:17]
	ds_read_b128 v[120:123], v99
	ds_read_b128 v[124:127], v119
	ds_read_b128 v[128:131], v119 offset:4096
	ds_read_b128 v[132:135], v118 offset:4096
	buffer_load_dwordx4 v72, s[4:7], s19 offen lds
	s_mov_b32 m0, s40
	s_nop 0
	buffer_load_dwordx4 v74, s[4:7], s19 offen lds
	s_mov_b32 m0, s41
	s_waitcnt lgkmcnt(2)
	v_mfma_f32_32x32x16_f16 v[50:65], v[120:123], v[124:127], v[50:65]
	buffer_load_dwordx4 v73, s[12:15], s19 offen lds
	s_mov_b32 m0, s42
	s_nop 0
	buffer_load_dwordx4 v75, s[12:15], s19 offen lds
	s_waitcnt vmcnt(8)
	s_barrier
	s_mov_b32 m0, s1
	s_waitcnt lgkmcnt(1)
	v_mfma_f32_32x32x16_f16 v[18:33], v[120:123], v[128:131], v[18:33]
	s_abs_i32 s1, s23
	s_waitcnt lgkmcnt(0)
	v_mfma_f32_32x32x16_f16 v[34:49], v[132:135], v[124:127], v[34:49]
	v_mfma_f32_32x32x16_f16 v[2:17], v[132:135], v[128:131], v[2:17]
	ds_read_b128 v[120:123], v110 offset:16384
	ds_read_b128 v[124:127], v111
	ds_read_b128 v[128:131], v111 offset:4096
	ds_read_b128 v[132:135], v110 offset:20480
	s_waitcnt lgkmcnt(2)
	v_mfma_f32_32x32x16_f16 v[50:65], v[120:123], v[124:127], v[50:65]
	s_waitcnt lgkmcnt(1)
	v_mfma_f32_32x32x16_f16 v[18:33], v[120:123], v[128:131], v[18:33]
	s_waitcnt lgkmcnt(0)
	v_mfma_f32_32x32x16_f16 v[34:49], v[132:135], v[124:127], v[34:49]
	v_mfma_f32_32x32x16_f16 v[2:17], v[132:135], v[128:131], v[2:17]
	ds_read_b128 v[120:123], v67 offset:16384
	ds_read_b128 v[124:127], v109
	ds_read_b128 v[128:131], v109 offset:4096
	ds_read_b128 v[132:135], v67 offset:20480
	buffer_load_dwordx4 v72, s[4:7], s31 offen lds
	s_mov_b32 m0, s2
	s_mul_hi_u32 s2, s1, s26
	buffer_load_dwordx4 v74, s[4:7], s31 offen lds
	s_mov_b32 m0, s3
	s_mul_i32 s3, s2, s24
	s_waitcnt lgkmcnt(2)
	v_mfma_f32_32x32x16_f16 v[50:65], v[120:123], v[124:127], v[50:65]
	buffer_load_dwordx4 v73, s[12:15], s31 offen lds
	s_mov_b32 m0, s18
	s_sub_i32 s1, s1, s3
	buffer_load_dwordx4 v75, s[12:15], s31 offen lds
	s_waitcnt vmcnt(8)
	s_barrier
	s_add_i32 s3, s2, 1
	s_waitcnt lgkmcnt(1)
	v_mfma_f32_32x32x16_f16 v[18:33], v[120:123], v[128:131], v[18:33]
	s_sub_i32 s14, s1, s24
	s_cmp_ge_u32 s1, s24
	s_cselect_b32 s2, s3, s2
	s_cselect_b32 s1, s14, s1
	s_add_i32 s3, s2, 1
	s_cmp_ge_u32 s1, s24
	s_cselect_b32 s1, s3, s2
	s_waitcnt lgkmcnt(0)
	v_mfma_f32_32x32x16_f16 v[34:49], v[132:135], v[124:127], v[34:49]
	s_xor_b32 s1, s1, s0
	s_sub_i32 s0, s1, s0
	s_mul_i32 s1, s0, s21
	s_sub_i32 s15, s23, s1
	s_lshl_b32 s2, s15, 7
	s_lshl_b32 s14, s0, 7
	s_ashr_i32 s3, s2, 31
	v_mfma_f32_32x32x16_f16 v[2:17], v[132:135], v[128:131], v[2:17]
	ds_read_b128 v[120:123], v110 offset:49152
	ds_read_b128 v[124:127], v111 offset:32768
	ds_read_b128 v[128:131], v111 offset:36864
	ds_read_b128 v[132:135], v110 offset:53248
	s_waitcnt lgkmcnt(2)
	v_mfma_f32_32x32x16_f16 v[50:65], v[120:123], v[124:127], v[50:65]
	s_waitcnt lgkmcnt(1)
	v_mfma_f32_32x32x16_f16 v[18:33], v[120:123], v[128:131], v[18:33]
	s_waitcnt lgkmcnt(0)
	v_mfma_f32_32x32x16_f16 v[34:49], v[132:135], v[124:127], v[34:49]
	v_mfma_f32_32x32x16_f16 v[2:17], v[132:135], v[128:131], v[2:17]
	ds_read_b128 v[120:123], v67 offset:49152
	ds_read_b128 v[124:127], v109 offset:32768
	ds_read_b128 v[128:131], v109 offset:36864
	ds_read_b128 v[132:135], v67 offset:53248
	s_waitcnt vmcnt(4)
	s_barrier
	s_waitcnt lgkmcnt(2)
	v_mfma_f32_32x32x16_f16 v[50:65], v[120:123], v[124:127], v[50:65]
	s_waitcnt lgkmcnt(1)
	v_mfma_f32_32x32x16_f16 v[18:33], v[120:123], v[128:131], v[18:33]
	s_waitcnt lgkmcnt(0)
	v_mfma_f32_32x32x16_f16 v[34:49], v[132:135], v[124:127], v[34:49]
	v_mfma_f32_32x32x16_f16 v[2:17], v[132:135], v[128:131], v[2:17]
	ds_read_b128 v[120:123], v96
	ds_read_b128 v[124:127], v113
	ds_read_b128 v[128:131], v113 offset:4096
	ds_read_b128 v[110:113], v112 offset:4096
	s_waitcnt lgkmcnt(2)
	v_mfma_f32_32x32x16_f16 v[50:65], v[120:123], v[124:127], v[50:65]
	s_waitcnt lgkmcnt(1)
	v_mfma_f32_32x32x16_f16 v[18:33], v[120:123], v[128:131], v[18:33]
	s_waitcnt lgkmcnt(0)
	v_mfma_f32_32x32x16_f16 v[34:49], v[110:113], v[124:127], v[34:49]
	ds_read_b128 v[120:123], v97
	ds_read_b128 v[124:127], v115
	ds_read_b128 v[132:135], v115 offset:4096
	s_waitcnt lgkmcnt(1)
	v_mfma_f32_32x32x16_f16 v[50:65], v[120:123], v[124:127], v[50:65]
	s_waitcnt lgkmcnt(0)
	v_mfma_f32_32x32x16_f16 v[18:33], v[120:123], v[132:135], v[18:33]
	ds_read_b128 v[120:123], v114 offset:4096
	s_waitcnt vmcnt(0)
	s_barrier
	v_mfma_f32_32x32x16_f16 v[2:17], v[110:113], v[128:131], v[2:17]
	s_waitcnt lgkmcnt(0)
	v_mfma_f32_32x32x16_f16 v[34:49], v[120:123], v[124:127], v[34:49]
	ds_read_b128 v[124:127], v98
	ds_read_b128 v[136:139], v117
	ds_read_b128 v[140:143], v117 offset:4096
	ds_read_b128 v[114:117], v116 offset:4096
	s_waitcnt lgkmcnt(2)
	v_mfma_f32_32x32x16_f16 v[50:65], v[124:127], v[136:139], v[50:65]
	s_waitcnt lgkmcnt(1)
	v_mfma_f32_32x32x16_f16 v[18:33], v[124:127], v[140:143], v[18:33]
	v_mfma_f32_32x32x16_f16 v[2:17], v[120:123], v[132:135], v[2:17]
	s_waitcnt lgkmcnt(0)
	v_mfma_f32_32x32x16_f16 v[34:49], v[114:117], v[136:139], v[34:49]
	ds_read_b128 v[124:127], v99
	ds_read_b128 v[136:139], v119
	ds_read_b128 v[144:147], v119 offset:4096
	s_waitcnt lgkmcnt(1)
	v_mfma_f32_32x32x16_f16 v[50:65], v[124:127], v[136:139], v[50:65]
	s_waitcnt lgkmcnt(0)
	v_mfma_f32_32x32x16_f16 v[18:33], v[124:127], v[144:147], v[18:33]
	ds_read_b128 v[124:127], v118 offset:4096
	s_waitcnt lgkmcnt(0)
	s_barrier
	s_nop 8
	ds_write_b128 v100, v[50:53]
	ds_write_b128 v101, v[54:57]
	v_mfma_f32_32x32x16_f16 v[2:17], v[114:117], v[140:143], v[2:17]
	s_waitcnt lgkmcnt(2)
	v_mfma_f32_32x32x16_f16 v[2:17], v[124:127], v[144:147], v[2:17]
	v_mfma_f32_32x32x16_f16 v[34:49], v[124:127], v[136:139], v[34:49]
	ds_write_b128 v102, v[58:61]
	ds_write_b128 v103, v[62:65]
	s_nop 9
	ds_write_b128 v104, v[34:37]
	ds_write_b128 v105, v[38:41]
	ds_write_b128 v106, v[42:45]
	ds_write_b128 v107, v[46:49]
	ds_write_b128 v100, v[18:21] offset:16384
	ds_write_b128 v101, v[22:25] offset:16384
	ds_write_b128 v102, v[26:29] offset:16384
	ds_write_b128 v103, v[30:33] offset:16384
	ds_write_b128 v104, v[2:5] offset:16384
	ds_write_b128 v105, v[6:9] offset:16384
	ds_write_b128 v106, v[10:13] offset:16384
	ds_write_b128 v107, v[14:17] offset:16384
	v_or_b32_e32 v25, s14, v1
	v_lshl_add_u64 v[22:23], s[2:3], 1, v[70:71]
	s_waitcnt lgkmcnt(0)
	s_barrier
	v_mad_i64_i32 v[2:3], s[0:1], v25, s29, v[22:23]
	v_mov_b64_e32 v[10:11], v[160:161]
	v_mov_b64_e32 v[12:13], v[162:163]
	v_lshl_add_u64 v[14:15], s[2:3], 2, v[68:69]
	v_mov_b64_e32 v[6:7], v[176:177]
	v_mov_b64_e32 v[8:9], v[178:179]
	v_mov_b64_e32 v[2:3], v[180:181]
	v_mov_b64_e32 v[4:5], v[182:183]
	v_add_u32_e32 v14, 0, v85
	v_add_u32_e32 v18, s28, v85
	ds_read_b128 v[14:17], v14
	ds_read_b128 v[26:29], v18
	v_or_b32_e32 v18, 32, v25
	v_mad_i64_i32 v[18:19], s[0:1], v18, s29, v[22:23]
	v_mov_b64_e32 v[18:19], v[164:165]
	v_mov_b64_e32 v[20:21], v[166:167]
	s_waitcnt lgkmcnt(0)
	v_pk_add_f32 v[16:17], v[16:17], v[28:29]
	v_add_f32_e32 v35, v14, v26
	v_mov_b32_e32 v34, v27
	v_xor_b32_e32 v24, 8, v108
	v_cvt_f32_f16_e32 v30, v11
	v_cvt_f32_f16_sdwa v31, v11 dst_sel:DWORD dst_unused:UNUSED_PAD src0_sel:WORD_1
	v_add_u32_e32 v11, 0, v86
	v_pk_add_f32 v[16:17], v[8:9], v[16:17]
	ds_read_b128 v[26:29], v11
	v_add_u32_e32 v11, s28, v86
	v_pk_add_f32 v[36:37], v[16:17], v[30:31]
	ds_read_b128 v[30:33], v11
	v_cvt_f32_f16_e32 v38, v13
	v_cvt_f32_f16_sdwa v39, v13 dst_sel:DWORD dst_unused:UNUSED_PAD src0_sel:WORD_1
	v_mov_b32_e32 v16, v2
	v_mov_b32_e32 v17, v3
	s_waitcnt lgkmcnt(0)
	v_pk_add_f32 v[28:29], v[28:29], v[32:33]
	v_cvt_f32_f16_e32 v32, v10
	v_pk_add_f32 v[28:29], v[4:5], v[28:29]
	v_pk_mov_b32 v[16:17], v[26:27], v[16:17] op_sel:[1,0]
	v_pk_add_f32 v[28:29], v[28:29], v[38:39]
	v_cvt_f32_f16_e32 v38, v12
	v_add_f32_e32 v26, v26, v30
	v_cvt_f32_f16_sdwa v33, v10 dst_sel:DWORD dst_unused:UNUSED_PAD src0_sel:WORD_1
	v_cvt_f32_f16_sdwa v30, v12 dst_sel:DWORD dst_unused:UNUSED_PAD src0_sel:WORD_1
	v_or_b32_e32 v12, 64, v25
	v_pk_mov_b32 v[14:15], v[14:15], v[6:7] op_sel:[1,0]
	v_mad_i64_i32 v[40:41], s[0:1], v12, s29, v[22:23]
	v_or_b32_e32 v12, 0x60, v25
	v_mov_b32_e32 v10, v31
	v_mov_b32_e32 v11, v26
	v_mad_i64_i32 v[42:43], s[0:1], v12, s29, v[22:23]
	v_pk_add_f32 v[44:45], v[14:15], v[34:35]
	v_mov_b32_e32 v12, v7
	v_mov_b32_e32 v13, v32
	v_pk_add_f32 v[10:11], v[16:17], v[10:11]
	v_pk_add_f32 v[46:47], v[12:13], v[44:45]
	v_mov_b32_e32 v22, v3
	v_mov_b32_e32 v23, v38
	v_pk_add_f32 v[48:49], v[22:23], v[10:11]
	v_mov_b32_e32 v10, v33
	v_mov_b32_e32 v11, v47
	v_pk_add_f32 v[50:51], v[46:47], v[10:11]
	v_mov_b64_e32 v[14:15], v[168:169]
	v_mov_b64_e32 v[16:17], v[170:171]
	v_mov_b64_e32 v[10:11], v[172:173]
	v_mov_b64_e32 v[12:13], v[174:175]
	v_mov_b32_e32 v31, v49
	v_pk_add_f32 v[40:41], v[48:49], v[30:31]
	v_pk_mov_b32 v[30:31], v[34:35], v[44:45] op_sel:[1,0]
	v_mov_b32_e32 v27, v44
	v_mov_b32_e32 v3, v7
	v_pk_add_f32 v[30:31], v[6:7], v[30:31]
	v_mov_b32_e32 v39, v33
	v_pk_add_f32 v[26:27], v[2:3], v[26:27]
	v_pk_add_f32 v[30:31], v[30:31], v[32:33]
	v_pk_add_f32 v[26:27], v[26:27], v[38:39]
	v_pk_mul_f32 v[32:33], v[46:47], v[46:47]
	v_pk_add_f32 v[34:35], v[30:31], v[26:27]
	v_pk_mul_f32 v[26:27], v[30:31], v[26:27]
	v_mov_b32_e32 v51, v33
	v_pk_mul_f32 v[32:33], v[48:49], v[48:49]
	v_mov_b32_e32 v35, v27
	v_pk_mul_f32 v[26:27], v[40:41], v[40:41]
	v_mov_b32_e32 v32, v40
	v_mov_b32_e32 v67, v26
	v_pk_add_f32 v[32:33], v[50:51], v[32:33]
	v_pk_add_f32 v[26:27], v[34:35], v[66:67]
	v_pk_mul_f32 v[30:31], v[36:37], v[36:37]
	v_pk_mul_f32 v[34:35], v[28:29], v[28:29]
	v_and_b32_e32 v23, 64, v108
	v_pk_add_f32 v[26:27], v[32:33], v[26:27]
	v_mov_b32_e32 v32, v36
	v_mov_b32_e32 v33, v30
	v_mov_b32_e32 v38, v28
	v_mov_b32_e32 v39, v34
	v_add_u32_e32 v23, 64, v23
	v_pk_add_f32 v[32:33], v[32:33], v[38:39]
	v_mov_b32_e32 v30, v37
	v_mov_b32_e32 v34, v29
	v_cmp_lt_i32_e64 s[0:1], v24, v23
	v_pk_add_f32 v[26:27], v[26:27], v[32:33]
	v_pk_add_f32 v[30:31], v[30:31], v[34:35]
	v_cndmask_b32_e64 v24, v108, v24, s[0:1]
	v_pk_add_f32 v[26:27], v[26:27], v[30:31]
	v_lshlrev_b32_e32 v30, 2, v24
	s_nop 1
	v_mov_b32_dpp v32, v26 row_mirror row_mask:0xf bank_mask:0xf
	v_mov_b32_dpp v33, v27 row_mirror row_mask:0xf bank_mask:0xf
	v_xor_b32_e32 v24, 4, v108
	v_cmp_lt_i32_e64 s[0:1], v24, v23
	v_cvt_pk_f16_f32 v39, v28, v29
	v_cvt_pk_f16_f32 v37, v36, v37
	v_cndmask_b32_e64 v24, v108, v24, s[0:1]
	s_waitcnt lgkmcnt(0)
	v_pk_add_f32 v[26:27], v[26:27], v[32:33]
	v_lshlrev_b32_e32 v31, 2, v24
	s_nop 1
	v_mov_b32_dpp v32, v26 row_half_mirror row_mask:0xf bank_mask:0xf
	v_mov_b32_dpp v33, v27 row_half_mirror row_mask:0xf bank_mask:0xf
	v_xor_b32_e32 v24, 2, v108
	v_cmp_lt_i32_e64 s[0:1], v24, v23
	v_cvt_pk_f16_f32 v36, v47, v50
	v_cvt_pk_f16_f32 v38, v49, v40
	v_cndmask_b32_e64 v24, v108, v24, s[0:1]
	s_waitcnt lgkmcnt(0)
	v_pk_add_f32 v[26:27], v[26:27], v[32:33]
	v_lshlrev_b32_e32 v33, 2, v24
	s_nop 1
	v_mov_b32_dpp v28, v26 quad_perm:[2,3,0,1] row_mask:0xf bank_mask:0xf
	v_mov_b32_dpp v29, v27 quad_perm:[2,3,0,1] row_mask:0xf bank_mask:0xf
	v_or_b32_e32 v32, s2, v78
	v_mul_lo_u32 v24, v25, s30
	v_add_lshl_u32 v24, v32, v24, 1
	buffer_store_dwordx4 v[36:39], v24, s[8:11], 0 offen sc1
	s_waitcnt lgkmcnt(0)
	v_pk_add_f32 v[26:27], v[26:27], v[28:29]
	v_xor_b32_e32 v28, 1, v108
	v_cmp_lt_i32_e64 s[0:1], v28, v23
	s_lshl_b32 s2, s15, 4
	v_mov_b32_e32 v24, v7
	v_cndmask_b32_e64 v23, v108, v28, s[0:1]
	v_lshlrev_b32_e32 v34, 2, v23
	s_nop 1
	v_mov_b32_dpp v28, v26 quad_perm:[1,0,3,2] row_mask:0xf bank_mask:0xf
	v_mov_b32_dpp v29, v27 quad_perm:[1,0,3,2] row_mask:0xf bank_mask:0xf
	s_and_saveexec_b64 s[0:1], vcc
	s_cbranch_execz .LBB9_5
	s_waitcnt lgkmcnt(0)
	v_pk_add_f32 v[64:65], v[26:27], v[28:29]
	v_lshl_add_u32 v23, v25, 6, s2
	v_mov_b32_e32 v67, v66
	s_mov_b32 s18, s10
	s_mov_b32 s19, s11
	buffer_store_dwordx4 v[64:67], v23, s[16:19], 0 offen sc1
.LBB9_5:
	s_or_b64 exec, exec, s[0:1]
	v_add_u32_e32 v23, 0, v88
	v_add_u32_e32 v25, s28, v88
	s_waitcnt lgkmcnt(0)
	ds_read_b128 v[26:29], v23
	ds_read_b128 v[36:39], v25
	v_add_u32_e32 v23, 0, v89
	v_add_u32_e32 v25, s28, v89
	ds_read_b128 v[40:43], v23
	ds_read_b128 v[44:47], v25
	v_cvt_f32_f16_e32 v50, v18
	s_waitcnt lgkmcnt(2)
	v_add_f32_e32 v49, v26, v36
	v_cvt_f32_f16_sdwa v51, v18 dst_sel:DWORD dst_unused:UNUSED_PAD src0_sel:WORD_1
	v_cvt_f32_f16_sdwa v55, v19 dst_sel:DWORD dst_unused:UNUSED_PAD src0_sel:WORD_1
	v_cvt_f32_f16_e32 v54, v19
	v_pk_mov_b32 v[26:27], v[26:27], v[6:7] op_sel:[1,0]
	v_mov_b32_e32 v48, v37
	v_cvt_f32_f16_e32 v52, v20
	v_pk_add_f32 v[26:27], v[26:27], v[48:49]
	v_pk_add_f32 v[28:29], v[28:29], v[38:39]
	v_pk_mov_b32 v[36:37], v[48:49], v[26:27] op_sel:[1,0]
	s_waitcnt lgkmcnt(0)
	v_add_f32_e32 v18, v40, v44
	v_pk_add_f32 v[28:29], v[8:9], v[28:29]
	v_pk_add_f32 v[36:37], v[6:7], v[36:37]
	v_mov_b32_e32 v25, v50
	v_cvt_f32_f16_sdwa v20, v20 dst_sel:DWORD dst_unused:UNUSED_PAD src0_sel:WORD_1
	v_pk_add_f32 v[28:29], v[28:29], v[54:55]
	v_mov_b32_e32 v19, v26
	v_pk_add_f32 v[54:55], v[24:25], v[26:27]
	v_pk_add_f32 v[26:27], v[36:37], v[50:51]
	v_pk_mov_b32 v[36:37], v[40:41], v[2:3] op_sel:[1,0]
	v_mov_b32_e32 v40, v45
	v_mov_b32_e32 v41, v18
	v_pk_add_f32 v[48:49], v[2:3], v[18:19]
	v_pk_add_f32 v[18:19], v[36:37], v[40:41]
	v_mov_b32_e32 v23, v52
	v_mov_b32_e32 v53, v51
	v_cvt_f32_f16_sdwa v57, v21 dst_sel:DWORD dst_unused:UNUSED_PAD src0_sel:WORD_1
	v_cvt_f32_f16_e32 v56, v21
	v_pk_add_f32 v[40:41], v[22:23], v[18:19]
	v_pk_add_f32 v[36:37], v[48:49], v[52:53]
	v_mov_b32_e32 v18, v51
	v_mov_b32_e32 v19, v55
	v_mov_b32_e32 v21, v41
	v_pk_add_f32 v[42:43], v[42:43], v[46:47]
	v_pk_add_f32 v[44:45], v[54:55], v[18:19]
	v_pk_mul_f32 v[18:19], v[54:55], v[54:55]
	v_pk_add_f32 v[48:49], v[40:41], v[20:21]
	v_pk_add_f32 v[20:21], v[26:27], v[36:37]
	v_pk_mul_f32 v[26:27], v[26:27], v[36:37]
	v_pk_add_f32 v[42:43], v[4:5], v[42:43]
	v_mov_b32_e32 v45, v19
	v_pk_mul_f32 v[18:19], v[40:41], v[40:41]
	v_mov_b32_e32 v21, v27
	v_pk_mul_f32 v[26:27], v[48:49], v[48:49]
	v_pk_add_f32 v[42:43], v[42:43], v[56:57]
	v_mov_b32_e32 v18, v48
	v_mov_b32_e32 v67, v26
	v_pk_mul_f32 v[38:39], v[28:29], v[28:29]
	v_pk_mul_f32 v[46:47], v[42:43], v[42:43]
	v_pk_add_f32 v[18:19], v[44:45], v[18:19]
	v_pk_add_f32 v[20:21], v[20:21], v[66:67]
	v_mov_b32_e32 v26, v42
	v_pk_add_f32 v[18:19], v[18:19], v[20:21]
	v_mov_b32_e32 v20, v28
	v_mov_b32_e32 v21, v38
	v_mov_b32_e32 v27, v46
	v_pk_add_f32 v[20:21], v[20:21], v[26:27]
	v_mov_b32_e32 v38, v29
	v_mov_b32_e32 v46, v43
	v_pk_add_f32 v[18:19], v[18:19], v[20:21]
	v_pk_add_f32 v[20:21], v[38:39], v[46:47]
	v_or_b32_e32 v23, s14, v87
	v_pk_add_f32 v[18:19], v[18:19], v[20:21]
	s_nop 1
	v_mov_b32_dpp v20, v18 row_mirror row_mask:0xf bank_mask:0xf
	v_mov_b32_dpp v21, v19 row_mirror row_mask:0xf bank_mask:0xf
	v_mul_lo_u32 v25, v23, s30
	v_cvt_pk_f16_f32 v27, v28, v29
	v_cvt_pk_f16_f32 v29, v42, v43
	v_add_lshl_u32 v25, v32, v25, 1
	s_waitcnt lgkmcnt(0)
	v_pk_add_f32 v[18:19], v[18:19], v[20:21]
	s_nop 1
	v_mov_b32_dpp v20, v18 row_half_mirror row_mask:0xf bank_mask:0xf
	v_mov_b32_dpp v21, v19 row_half_mirror row_mask:0xf bank_mask:0xf
	v_cvt_pk_f16_f32 v26, v55, v44
	v_cvt_pk_f16_f32 v28, v41, v48
	buffer_store_dwordx4 v[26:29], v25, s[8:11], 0 offen sc1
	s_waitcnt lgkmcnt(0)
	v_pk_add_f32 v[18:19], v[18:19], v[20:21]
	s_nop 1
	v_mov_b32_dpp v20, v18 quad_perm:[2,3,0,1] row_mask:0xf bank_mask:0xf
	v_mov_b32_dpp v21, v19 quad_perm:[2,3,0,1] row_mask:0xf bank_mask:0xf
	s_waitcnt lgkmcnt(0)
	v_pk_add_f32 v[18:19], v[18:19], v[20:21]
	s_nop 1
	v_mov_b32_dpp v20, v18 quad_perm:[1,0,3,2] row_mask:0xf bank_mask:0xf
	v_mov_b32_dpp v21, v19 quad_perm:[1,0,3,2] row_mask:0xf bank_mask:0xf
	s_and_saveexec_b64 s[0:1], vcc
	s_cbranch_execz .LBB9_7
	s_waitcnt lgkmcnt(0)
	v_pk_add_f32 v[64:65], v[18:19], v[20:21]
	v_lshl_add_u32 v18, v23, 6, s2
	v_mov_b32_e32 v67, v66
	s_mov_b32 s18, s10
	s_mov_b32 s19, s11
	buffer_store_dwordx4 v[64:67], v18, s[16:19], 0 offen sc1
.LBB9_7:
	s_or_b64 exec, exec, s[0:1]
	v_add_u32_e32 v18, 0, v91
	v_add_u32_e32 v23, s28, v91
	s_waitcnt lgkmcnt(0)
	ds_read_b128 v[18:21], v18
	ds_read_b128 v[26:29], v23
	v_add_u32_e32 v23, 0, v92
	v_add_u32_e32 v25, s28, v92
	ds_read_b128 v[36:39], v23
	ds_read_b128 v[40:43], v25
	v_cvt_f32_f16_e32 v46, v14
	v_cvt_f32_f16_e32 v48, v16
	s_waitcnt lgkmcnt(2)
	v_add_f32_e32 v45, v18, v26
	v_cvt_f32_f16_sdwa v47, v14 dst_sel:DWORD dst_unused:UNUSED_PAD src0_sel:WORD_1
	v_pk_mov_b32 v[18:19], v[18:19], v[6:7] op_sel:[1,0]
	v_mov_b32_e32 v44, v27
	s_waitcnt lgkmcnt(0)
	v_add_f32_e32 v14, v36, v40
	v_pk_add_f32 v[18:19], v[18:19], v[44:45]
	v_cvt_f32_f16_sdwa v16, v16 dst_sel:DWORD dst_unused:UNUSED_PAD src0_sel:WORD_1
	v_cvt_f32_f16_sdwa v51, v15 dst_sel:DWORD dst_unused:UNUSED_PAD src0_sel:WORD_1
	v_cvt_f32_f16_e32 v50, v15
	v_mov_b32_e32 v15, v18
	v_pk_mov_b32 v[36:37], v[36:37], v[2:3] op_sel:[1,0]
	v_mov_b32_e32 v40, v41
	v_mov_b32_e32 v41, v14
	v_pk_mov_b32 v[26:27], v[44:45], v[18:19] op_sel:[1,0]
	v_pk_add_f32 v[44:45], v[2:3], v[14:15]
	v_mov_b32_e32 v25, v46
	v_pk_add_f32 v[14:15], v[36:37], v[40:41]
	v_mov_b32_e32 v23, v48
	v_mov_b32_e32 v49, v47
	v_cvt_f32_f16_sdwa v53, v17 dst_sel:DWORD dst_unused:UNUSED_PAD src0_sel:WORD_1
	v_cvt_f32_f16_e32 v52, v17
	v_pk_add_f32 v[26:27], v[6:7], v[26:27]
	v_pk_add_f32 v[18:19], v[24:25], v[18:19]
	v_pk_add_f32 v[40:41], v[22:23], v[14:15]
	v_pk_add_f32 v[26:27], v[26:27], v[46:47]
	v_pk_add_f32 v[36:37], v[44:45], v[48:49]
	v_mov_b32_e32 v14, v47
	v_mov_b32_e32 v15, v19
	v_mov_b32_e32 v17, v41
	v_pk_add_f32 v[20:21], v[20:21], v[28:29]
	v_pk_add_f32 v[38:39], v[38:39], v[42:43]
	v_pk_add_f32 v[44:45], v[18:19], v[14:15]
	v_pk_mul_f32 v[14:15], v[18:19], v[18:19]
	v_pk_add_f32 v[46:47], v[40:41], v[16:17]
	v_pk_add_f32 v[16:17], v[26:27], v[36:37]
	v_pk_mul_f32 v[26:27], v[26:27], v[36:37]
	v_pk_add_f32 v[20:21], v[8:9], v[20:21]
	v_pk_add_f32 v[38:39], v[4:5], v[38:39]
	v_mov_b32_e32 v45, v15
	v_pk_mul_f32 v[14:15], v[40:41], v[40:41]
	v_mov_b32_e32 v17, v27
	v_pk_mul_f32 v[26:27], v[46:47], v[46:47]
	v_pk_add_f32 v[20:21], v[20:21], v[50:51]
	v_pk_add_f32 v[38:39], v[38:39], v[52:53]
	v_mov_b32_e32 v14, v46
	v_mov_b32_e32 v67, v26
	v_pk_mul_f32 v[28:29], v[20:21], v[20:21]
	v_pk_mul_f32 v[42:43], v[38:39], v[38:39]
	v_pk_add_f32 v[14:15], v[44:45], v[14:15]
	v_pk_add_f32 v[16:17], v[16:17], v[66:67]
	v_mov_b32_e32 v26, v38
	v_pk_add_f32 v[14:15], v[14:15], v[16:17]
	v_mov_b32_e32 v16, v20
	v_mov_b32_e32 v17, v28
	v_mov_b32_e32 v27, v42
	v_pk_add_f32 v[16:17], v[16:17], v[26:27]
	v_mov_b32_e32 v28, v21
	v_mov_b32_e32 v42, v39
	v_pk_add_f32 v[14:15], v[14:15], v[16:17]
	v_pk_add_f32 v[16:17], v[28:29], v[42:43]
	v_or_b32_e32 v18, s14, v90
	v_pk_add_f32 v[14:15], v[14:15], v[16:17]
	s_nop 1
	v_mov_b32_dpp v16, v14 row_mirror row_mask:0xf bank_mask:0xf
	v_mov_b32_dpp v17, v15 row_mirror row_mask:0xf bank_mask:0xf
	v_cvt_pk_f16_f32 v27, v20, v21
	v_mul_lo_u32 v20, v18, s30
	v_cvt_pk_f16_f32 v29, v38, v39
	v_add_lshl_u32 v20, v32, v20, 1
	s_waitcnt lgkmcnt(0)
	v_pk_add_f32 v[14:15], v[14:15], v[16:17]
	s_nop 1
	v_mov_b32_dpp v16, v14 row_half_mirror row_mask:0xf bank_mask:0xf
	v_mov_b32_dpp v17, v15 row_half_mirror row_mask:0xf bank_mask:0xf
	v_cvt_pk_f16_f32 v26, v19, v44
	v_cvt_pk_f16_f32 v28, v41, v46
	buffer_store_dwordx4 v[26:29], v20, s[8:11], 0 offen sc1
	s_waitcnt lgkmcnt(0)
	v_pk_add_f32 v[14:15], v[14:15], v[16:17]
	s_nop 1
	v_mov_b32_dpp v16, v14 quad_perm:[2,3,0,1] row_mask:0xf bank_mask:0xf
	v_mov_b32_dpp v17, v15 quad_perm:[2,3,0,1] row_mask:0xf bank_mask:0xf
	s_waitcnt lgkmcnt(0)
	v_pk_add_f32 v[14:15], v[14:15], v[16:17]
	s_nop 1
	v_mov_b32_dpp v16, v14 quad_perm:[1,0,3,2] row_mask:0xf bank_mask:0xf
	v_mov_b32_dpp v17, v15 quad_perm:[1,0,3,2] row_mask:0xf bank_mask:0xf
	s_and_saveexec_b64 s[0:1], vcc
	s_cbranch_execz .LBB9_9
	s_waitcnt lgkmcnt(0)
	v_pk_add_f32 v[64:65], v[14:15], v[16:17]
	v_lshl_add_u32 v14, v18, 6, s2
	v_mov_b32_e32 v67, v66
	s_mov_b32 s18, s10
	s_mov_b32 s19, s11
	buffer_store_dwordx4 v[64:67], v14, s[16:19], 0 offen sc1
.LBB9_9:
	s_or_b64 exec, exec, s[0:1]
	v_add_u32_e32 v14, 0, v94
	v_add_u32_e32 v18, s28, v94
	s_waitcnt lgkmcnt(0)
	ds_read_b128 v[14:17], v14
	ds_read_b128 v[18:21], v18
	v_add_u32_e32 v23, 0, v95
	v_add_u32_e32 v25, s28, v95
	ds_read_b128 v[26:29], v23
	ds_read_b128 v[36:39], v25
	v_cvt_f32_f16_e32 v42, v10
	s_waitcnt lgkmcnt(2)
	v_add_f32_e32 v41, v14, v18
	v_cvt_f32_f16_sdwa v43, v10 dst_sel:DWORD dst_unused:UNUSED_PAD src0_sel:WORD_1
	v_cvt_f32_f16_e32 v44, v12
	v_pk_mov_b32 v[14:15], v[14:15], v[6:7] op_sel:[1,0]
	v_mov_b32_e32 v40, v19
	v_pk_add_f32 v[14:15], v[14:15], v[40:41]
	s_waitcnt lgkmcnt(0)
	v_add_f32_e32 v10, v26, v36
	v_cvt_f32_f16_sdwa v47, v11 dst_sel:DWORD dst_unused:UNUSED_PAD src0_sel:WORD_1
	v_cvt_f32_f16_e32 v46, v11
	v_pk_mov_b32 v[18:19], v[40:41], v[14:15] op_sel:[1,0]
	v_mov_b32_e32 v11, v14
	v_mov_b32_e32 v25, v42
	v_cvt_f32_f16_sdwa v12, v12 dst_sel:DWORD dst_unused:UNUSED_PAD src0_sel:WORD_1
	v_pk_add_f32 v[6:7], v[6:7], v[18:19]
	v_pk_add_f32 v[18:19], v[2:3], v[10:11]
	v_pk_add_f32 v[14:15], v[24:25], v[14:15]
	v_pk_mov_b32 v[2:3], v[26:27], v[2:3] op_sel:[1,0]
	v_mov_b32_e32 v24, v37
	v_mov_b32_e32 v25, v10
	v_mov_b32_e32 v45, v43
	v_pk_add_f32 v[2:3], v[2:3], v[24:25]
	v_mov_b32_e32 v23, v44
	v_cvt_f32_f16_sdwa v49, v13 dst_sel:DWORD dst_unused:UNUSED_PAD src0_sel:WORD_1
	v_cvt_f32_f16_e32 v48, v13
	v_pk_add_f32 v[10:11], v[18:19], v[44:45]
	v_pk_add_f32 v[18:19], v[22:23], v[2:3]
	v_pk_add_f32 v[6:7], v[6:7], v[42:43]
	v_mov_b32_e32 v2, v43
	v_mov_b32_e32 v3, v15
	v_mov_b32_e32 v13, v19
	v_pk_add_f32 v[16:17], v[16:17], v[20:21]
	v_pk_add_f32 v[20:21], v[28:29], v[38:39]
	v_pk_add_f32 v[22:23], v[14:15], v[2:3]
	v_pk_mul_f32 v[2:3], v[14:15], v[14:15]
	v_pk_add_f32 v[12:13], v[18:19], v[12:13]
	v_pk_add_f32 v[24:25], v[6:7], v[10:11]
	v_pk_mul_f32 v[6:7], v[6:7], v[10:11]
	v_pk_add_f32 v[8:9], v[8:9], v[16:17]
	v_pk_add_f32 v[4:5], v[4:5], v[20:21]
	v_mov_b32_e32 v23, v3
	v_pk_mul_f32 v[2:3], v[18:19], v[18:19]
	v_mov_b32_e32 v25, v7
	v_pk_mul_f32 v[6:7], v[12:13], v[12:13]
	v_pk_add_f32 v[8:9], v[8:9], v[46:47]
	v_pk_add_f32 v[4:5], v[4:5], v[48:49]
	v_mov_b32_e32 v2, v12
	v_mov_b32_e32 v67, v6
	v_pk_mul_f32 v[16:17], v[8:9], v[8:9]
	v_pk_mul_f32 v[20:21], v[4:5], v[4:5]
	v_pk_add_f32 v[2:3], v[22:23], v[2:3]
	v_pk_add_f32 v[6:7], v[24:25], v[66:67]
	v_mov_b32_e32 v10, v4
	v_pk_add_f32 v[2:3], v[2:3], v[6:7]
	v_mov_b32_e32 v6, v8
	v_mov_b32_e32 v7, v16
	v_mov_b32_e32 v11, v20
	v_pk_add_f32 v[6:7], v[6:7], v[10:11]
	v_mov_b32_e32 v16, v9
	v_mov_b32_e32 v20, v5
	v_pk_add_f32 v[2:3], v[2:3], v[6:7]
	v_pk_add_f32 v[6:7], v[16:17], v[20:21]
	v_cvt_pk_f16_f32 v11, v4, v5
	v_pk_add_f32 v[2:3], v[2:3], v[6:7]
	s_nop 1
	v_mov_b32_dpp v6, v2 row_mirror row_mask:0xf bank_mask:0xf
	v_mov_b32_dpp v7, v3 row_mirror row_mask:0xf bank_mask:0xf
	v_cvt_pk_f16_f32 v9, v8, v9
	v_cvt_pk_f16_f32 v8, v15, v22
	v_cvt_pk_f16_f32 v10, v19, v12
	s_waitcnt lgkmcnt(0)
	v_pk_add_f32 v[2:3], v[2:3], v[6:7]
	s_nop 1
	v_mov_b32_dpp v6, v2 row_half_mirror row_mask:0xf bank_mask:0xf
	v_mov_b32_dpp v7, v3 row_half_mirror row_mask:0xf bank_mask:0xf
	s_waitcnt lgkmcnt(0)
	v_pk_add_f32 v[2:3], v[2:3], v[6:7]
	s_nop 1
	v_mov_b32_dpp v16, v2 quad_perm:[2,3,0,1] row_mask:0xf bank_mask:0xf
	v_mov_b32_dpp v17, v3 quad_perm:[2,3,0,1] row_mask:0xf bank_mask:0xf
	v_add_u32_e32 v6, s14, v93
	v_mul_lo_u32 v7, v6, s30
	v_add_lshl_u32 v7, v32, v7, 1
	buffer_store_dwordx4 v[8:11], v7, s[8:11], 0 offen sc1
	s_waitcnt lgkmcnt(0)
	v_pk_add_f32 v[2:3], v[2:3], v[16:17]
	s_nop 1
	v_mov_b32_dpp v4, v2 quad_perm:[1,0,3,2] row_mask:0xf bank_mask:0xf
	v_mov_b32_dpp v5, v3 quad_perm:[1,0,3,2] row_mask:0xf bank_mask:0xf
	s_and_saveexec_b64 s[0:1], vcc
	s_cbranch_execz .LBB9_2
	s_waitcnt lgkmcnt(0)
	v_pk_add_f32 v[64:65], v[2:3], v[4:5]
	v_lshl_add_u32 v2, v6, 6, s2
	v_mov_b32_e32 v67, v66
	s_mov_b32 s18, s10
	s_mov_b32 s19, s11
	buffer_store_dwordx4 v[64:67], v2, s[16:19], 0 offen sc1
	s_branch .LBB9_2
